# indexer scratch holds the top 24 bits of each score (exactly what pass B reads), 1.5 KiB per group so more groups fit; unpacked by v_perm in the stored-score loop
# speedup vs baseline: 1.0459x; 1.0064x over previous
.LBB0_1297:
	v_readlane_b32 s14, v254, 48
	v_readlane_b32 s15, v254, 49
	s_andn2_b64 vcc, exec, s[14:15]
	s_cbranch_vccnz .LBB0_1558
	s_waitcnt lgkmcnt(0)
	s_add_u32 s22, s20, 0x2c200000
	s_addc_u32 s23, s21, 0
	s_add_u32 s18, s20, 0x3f700000
	s_addc_u32 s19, s21, 0
	s_add_u32 s24, s20, 0x2c400000
	s_addc_u32 s25, s21, 0
	s_add_u32 s26, s20, 0x2b200000
	v_readlane_b32 s14, v255, 0
	s_addc_u32 s27, s21, 0
	s_mov_b32 s76, s14
	s_lshr_b32 s32, s14, 1
	s_sub_i32 s100, 403, s32
	s_add_i32 s101, s32, -1
	s_mul_i32 s101, s101, s32
	s_bitcmp1_b32 s14, 0
	s_cselect_b32 s32, s32, 0
	s_add_i32 s101, s101, s32
	s_mul_i32 s32, s14, 404
	s_sub_i32 s101, s32, s101
	s_mul_i32 s101, s101, 0x600
	s_add_u32 s101, s101, 0x35d00000
	v_mbcnt_lo_u32_b32 v230, -1, 0
	v_mbcnt_hi_u32_b32 v230, -1, v230
	v_lshlrev_b32_e32 v197, 3, v230
	v_lshlrev_b32_e32 v230, 4, v230
	v_add_u32_e32 v230, s101, v230
	v_add_u32_e32 v197, s101, v197
	v_add_u32_e32 v197, 0x400, v197
	v_readlane_b32 s15, v255, 1
	s_branch .LBB0_1300

.LBB0_1302:
	s_and_b64 s[14:15], s[28:29], exec
	s_cselect_b32 s14, s77, s76
	s_lshl_b32 s34, s14, 4
	s_mov_b32 s14, s33
	s_nop 0
	v_lshl_or_b32 v72, s14, 6, v195
	s_nop 0
	v_readfirstlane_b32 s14, v72
	s_ashr_i32 s30, s14, 6
	s_and_b32 s14, s34, 0xffffffc0
	s_add_i32 s14, s14, 64
	s_ashr_i32 s82, s14, 5
	v_and_b32_e32 v126, 63, v72
	v_and_b32_e32 v125, 15, v72
	s_cmpk_gt_i32 s14, 0x100
	s_mov_b64 s[14:15], -1
	s_cbranch_scc0 .LBB0_1545
	v_or_b32_e32 v0, s34, v125
	v_ashrrev_i32_e32 v1, 31, v0
	v_lshlrev_b64 v[2:3], 10, v[0:1]
	v_lshl_add_u64 v[2:3], s[26:27], 0, v[2:3]
	v_and_b32_e32 v176, 48, v126
	v_lshlrev_b64 v[0:1], 5, v[0:1]
	v_lshl_add_u64 v[68:69], v[2:3], 0, v[176:177]
	v_lshl_add_u64 v[12:13], s[24:25], 0, v[0:1]
	global_load_dwordx4 v[0:3], v[68:69], off
	global_load_dwordx4 v[4:7], v[68:69], off offset:64
	global_load_dwordx4 v[8:11], v[12:13], off offset:16
	s_nop 0
	global_load_dwordx4 v[12:15], v[12:13], off
	s_nop 0
	global_load_dwordx4 v[16:19], v[68:69], off offset:128
	global_load_dwordx4 v[20:23], v[68:69], off offset:192
	global_load_dwordx4 v[24:27], v[68:69], off offset:256
	global_load_dwordx4 v[28:31], v[68:69], off offset:320
	global_load_dwordx4 v[32:35], v[68:69], off offset:384
	global_load_dwordx4 v[36:39], v[68:69], off offset:448
	global_load_dwordx4 v[40:43], v[68:69], off offset:512
	global_load_dwordx4 v[44:47], v[68:69], off offset:576
	global_load_dwordx4 v[48:51], v[68:69], off offset:640
	global_load_dwordx4 v[52:55], v[68:69], off offset:704
	global_load_dwordx4 v[56:59], v[68:69], off offset:768
	global_load_dwordx4 v[60:63], v[68:69], off offset:832
	global_load_dwordx4 v[64:67], v[68:69], off offset:896
	s_nop 0
	global_load_dwordx4 v[68:71], v[68:69], off offset:960
	s_mov_b32 s74, s73
	s_mov_b32 s75, s73
	v_lshlrev_b32_e32 v73, 4, v72
	s_mov_b32 s72, s73
	v_mov_b64_e32 v[76:77], s[74:75]
	v_add_u32_e32 v122, 0, v73
	v_mov_b64_e32 v[74:75], s[72:73]
	v_cmp_gt_i32_e32 vcc, 17, v72
	s_waitcnt vmcnt(0)
	v_mul_f32_e32 v8, 0.5, v8
	v_mul_f32_e32 v9, 0.5, v9
	v_mul_f32_e32 v10, 0.5, v10
	v_mul_f32_e32 v11, 0.5, v11
	v_mul_f32_e32 v12, 0.5, v12
	v_mul_f32_e32 v13, 0.5, v13
	v_mul_f32_e32 v14, 0.5, v14
	v_mul_f32_e32 v15, 0.5, v15
	v_lshlrev_b32_e32 v206, 16, v0
	v_and_b32_e32 v207, 0xffff0000, v0
	v_mul_f32_e32 v208, v12, v206
	v_mul_f32_e32 v209, v12, v207
	v_lshlrev_b32_e32 v206, 16, v16
	v_and_b32_e32 v207, 0xffff0000, v16
	v_fmac_f32_e32 v208, v13, v206
	v_fmac_f32_e32 v209, v13, v207
	v_lshlrev_b32_e32 v206, 16, v24
	v_and_b32_e32 v207, 0xffff0000, v24
	v_fmac_f32_e32 v208, v14, v206
	v_fmac_f32_e32 v209, v14, v207
	v_lshlrev_b32_e32 v206, 16, v32
	v_and_b32_e32 v207, 0xffff0000, v32
	v_fmac_f32_e32 v208, v15, v206
	v_fmac_f32_e32 v209, v15, v207
	v_lshlrev_b32_e32 v206, 16, v40
	v_and_b32_e32 v207, 0xffff0000, v40
	v_fmac_f32_e32 v208, v8, v206
	v_fmac_f32_e32 v209, v8, v207
	v_lshlrev_b32_e32 v206, 16, v48
	v_and_b32_e32 v207, 0xffff0000, v48
	v_fmac_f32_e32 v208, v9, v206
	v_fmac_f32_e32 v209, v9, v207
	v_lshlrev_b32_e32 v206, 16, v56
	v_and_b32_e32 v207, 0xffff0000, v56
	v_fmac_f32_e32 v208, v10, v206
	v_fmac_f32_e32 v209, v10, v207
	v_lshlrev_b32_e32 v206, 16, v64
	v_and_b32_e32 v207, 0xffff0000, v64
	v_fmac_f32_e32 v208, v11, v206
	v_fmac_f32_e32 v209, v11, v207
	v_cvt_pk_bf16_f32 v244, v208, v209
	v_lshlrev_b32_e32 v206, 16, v1
	v_and_b32_e32 v207, 0xffff0000, v1
	v_mul_f32_e32 v208, v12, v206
	v_mul_f32_e32 v209, v12, v207
	v_lshlrev_b32_e32 v206, 16, v17
	v_and_b32_e32 v207, 0xffff0000, v17
	v_fmac_f32_e32 v208, v13, v206
	v_fmac_f32_e32 v209, v13, v207
	v_lshlrev_b32_e32 v206, 16, v25
	v_and_b32_e32 v207, 0xffff0000, v25
	v_fmac_f32_e32 v208, v14, v206
	v_fmac_f32_e32 v209, v14, v207
	v_lshlrev_b32_e32 v206, 16, v33
	v_and_b32_e32 v207, 0xffff0000, v33
	v_fmac_f32_e32 v208, v15, v206
	v_fmac_f32_e32 v209, v15, v207
	v_lshlrev_b32_e32 v206, 16, v41
	v_and_b32_e32 v207, 0xffff0000, v41
	v_fmac_f32_e32 v208, v8, v206
	v_fmac_f32_e32 v209, v8, v207
	v_lshlrev_b32_e32 v206, 16, v49
	v_and_b32_e32 v207, 0xffff0000, v49
	v_fmac_f32_e32 v208, v9, v206
	v_fmac_f32_e32 v209, v9, v207
	v_lshlrev_b32_e32 v206, 16, v57
	v_and_b32_e32 v207, 0xffff0000, v57
	v_fmac_f32_e32 v208, v10, v206
	v_fmac_f32_e32 v209, v10, v207
	v_lshlrev_b32_e32 v206, 16, v65
	v_and_b32_e32 v207, 0xffff0000, v65
	v_fmac_f32_e32 v208, v11, v206
	v_fmac_f32_e32 v209, v11, v207
	v_cvt_pk_bf16_f32 v245, v208, v209
	v_lshlrev_b32_e32 v206, 16, v2
	v_and_b32_e32 v207, 0xffff0000, v2
	v_mul_f32_e32 v208, v12, v206
	v_mul_f32_e32 v209, v12, v207
	v_lshlrev_b32_e32 v206, 16, v18
	v_and_b32_e32 v207, 0xffff0000, v18
	v_fmac_f32_e32 v208, v13, v206
	v_fmac_f32_e32 v209, v13, v207
	v_lshlrev_b32_e32 v206, 16, v26
	v_and_b32_e32 v207, 0xffff0000, v26
	v_fmac_f32_e32 v208, v14, v206
	v_fmac_f32_e32 v209, v14, v207
	v_lshlrev_b32_e32 v206, 16, v34
	v_and_b32_e32 v207, 0xffff0000, v34
	v_fmac_f32_e32 v208, v15, v206
	v_fmac_f32_e32 v209, v15, v207
	v_lshlrev_b32_e32 v206, 16, v42
	v_and_b32_e32 v207, 0xffff0000, v42
	v_fmac_f32_e32 v208, v8, v206
	v_fmac_f32_e32 v209, v8, v207
	v_lshlrev_b32_e32 v206, 16, v50
	v_and_b32_e32 v207, 0xffff0000, v50
	v_fmac_f32_e32 v208, v9, v206
	v_fmac_f32_e32 v209, v9, v207
	v_lshlrev_b32_e32 v206, 16, v58
	v_and_b32_e32 v207, 0xffff0000, v58
	v_fmac_f32_e32 v208, v10, v206
	v_fmac_f32_e32 v209, v10, v207
	v_lshlrev_b32_e32 v206, 16, v66
	v_and_b32_e32 v207, 0xffff0000, v66
	v_fmac_f32_e32 v208, v11, v206
	v_fmac_f32_e32 v209, v11, v207
	v_cvt_pk_bf16_f32 v246, v208, v209
	v_lshlrev_b32_e32 v206, 16, v3
	v_and_b32_e32 v207, 0xffff0000, v3
	v_mul_f32_e32 v208, v12, v206
	v_mul_f32_e32 v209, v12, v207
	v_lshlrev_b32_e32 v206, 16, v19
	v_and_b32_e32 v207, 0xffff0000, v19
	v_fmac_f32_e32 v208, v13, v206
	v_fmac_f32_e32 v209, v13, v207
	v_lshlrev_b32_e32 v206, 16, v27
	v_and_b32_e32 v207, 0xffff0000, v27
	v_fmac_f32_e32 v208, v14, v206
	v_fmac_f32_e32 v209, v14, v207
	v_lshlrev_b32_e32 v206, 16, v35
	v_and_b32_e32 v207, 0xffff0000, v35
	v_fmac_f32_e32 v208, v15, v206
	v_fmac_f32_e32 v209, v15, v207
	v_lshlrev_b32_e32 v206, 16, v43
	v_and_b32_e32 v207, 0xffff0000, v43
	v_fmac_f32_e32 v208, v8, v206
	v_fmac_f32_e32 v209, v8, v207
	v_lshlrev_b32_e32 v206, 16, v51
	v_and_b32_e32 v207, 0xffff0000, v51
	v_fmac_f32_e32 v208, v9, v206
	v_fmac_f32_e32 v209, v9, v207
	v_lshlrev_b32_e32 v206, 16, v59
	v_and_b32_e32 v207, 0xffff0000, v59
	v_fmac_f32_e32 v208, v10, v206
	v_fmac_f32_e32 v209, v10, v207
	v_lshlrev_b32_e32 v206, 16, v67
	v_and_b32_e32 v207, 0xffff0000, v67
	v_fmac_f32_e32 v208, v11, v206
	v_fmac_f32_e32 v209, v11, v207
	v_cvt_pk_bf16_f32 v247, v208, v209
	v_lshlrev_b32_e32 v206, 16, v4
	v_and_b32_e32 v207, 0xffff0000, v4
	v_mul_f32_e32 v208, v12, v206
	v_mul_f32_e32 v209, v12, v207
	v_lshlrev_b32_e32 v206, 16, v20
	v_and_b32_e32 v207, 0xffff0000, v20
	v_fmac_f32_e32 v208, v13, v206
	v_fmac_f32_e32 v209, v13, v207
	v_lshlrev_b32_e32 v206, 16, v28
	v_and_b32_e32 v207, 0xffff0000, v28
	v_fmac_f32_e32 v208, v14, v206
	v_fmac_f32_e32 v209, v14, v207
	v_lshlrev_b32_e32 v206, 16, v36
	v_and_b32_e32 v207, 0xffff0000, v36
	v_fmac_f32_e32 v208, v15, v206
	v_fmac_f32_e32 v209, v15, v207
	v_lshlrev_b32_e32 v206, 16, v44
	v_and_b32_e32 v207, 0xffff0000, v44
	v_fmac_f32_e32 v208, v8, v206
	v_fmac_f32_e32 v209, v8, v207
	v_lshlrev_b32_e32 v206, 16, v52
	v_and_b32_e32 v207, 0xffff0000, v52
	v_fmac_f32_e32 v208, v9, v206
	v_fmac_f32_e32 v209, v9, v207
	v_lshlrev_b32_e32 v206, 16, v60
	v_and_b32_e32 v207, 0xffff0000, v60
	v_fmac_f32_e32 v208, v10, v206
	v_fmac_f32_e32 v209, v10, v207
	v_lshlrev_b32_e32 v206, 16, v68
	v_and_b32_e32 v207, 0xffff0000, v68
	v_fmac_f32_e32 v208, v11, v206
	v_fmac_f32_e32 v209, v11, v207
	v_cvt_pk_bf16_f32 v248, v208, v209
	v_lshlrev_b32_e32 v206, 16, v5
	v_and_b32_e32 v207, 0xffff0000, v5
	v_mul_f32_e32 v208, v12, v206
	v_mul_f32_e32 v209, v12, v207
	v_lshlrev_b32_e32 v206, 16, v21
	v_and_b32_e32 v207, 0xffff0000, v21
	v_fmac_f32_e32 v208, v13, v206
	v_fmac_f32_e32 v209, v13, v207
	v_lshlrev_b32_e32 v206, 16, v29
	v_and_b32_e32 v207, 0xffff0000, v29
	v_fmac_f32_e32 v208, v14, v206
	v_fmac_f32_e32 v209, v14, v207
	v_lshlrev_b32_e32 v206, 16, v37
	v_and_b32_e32 v207, 0xffff0000, v37
	v_fmac_f32_e32 v208, v15, v206
	v_fmac_f32_e32 v209, v15, v207
	v_lshlrev_b32_e32 v206, 16, v45
	v_and_b32_e32 v207, 0xffff0000, v45
	v_fmac_f32_e32 v208, v8, v206
	v_fmac_f32_e32 v209, v8, v207
	v_lshlrev_b32_e32 v206, 16, v53
	v_and_b32_e32 v207, 0xffff0000, v53
	v_fmac_f32_e32 v208, v9, v206
	v_fmac_f32_e32 v209, v9, v207
	v_lshlrev_b32_e32 v206, 16, v61
	v_and_b32_e32 v207, 0xffff0000, v61
	v_fmac_f32_e32 v208, v10, v206
	v_fmac_f32_e32 v209, v10, v207
	v_lshlrev_b32_e32 v206, 16, v69
	v_and_b32_e32 v207, 0xffff0000, v69
	v_fmac_f32_e32 v208, v11, v206
	v_fmac_f32_e32 v209, v11, v207
	v_cvt_pk_bf16_f32 v249, v208, v209
	v_lshlrev_b32_e32 v206, 16, v6
	v_and_b32_e32 v207, 0xffff0000, v6
	v_mul_f32_e32 v208, v12, v206
	v_mul_f32_e32 v209, v12, v207
	v_lshlrev_b32_e32 v206, 16, v22
	v_and_b32_e32 v207, 0xffff0000, v22
	v_fmac_f32_e32 v208, v13, v206
	v_fmac_f32_e32 v209, v13, v207
	v_lshlrev_b32_e32 v206, 16, v30
	v_and_b32_e32 v207, 0xffff0000, v30
	v_fmac_f32_e32 v208, v14, v206
	v_fmac_f32_e32 v209, v14, v207
	v_lshlrev_b32_e32 v206, 16, v38
	v_and_b32_e32 v207, 0xffff0000, v38
	v_fmac_f32_e32 v208, v15, v206
	v_fmac_f32_e32 v209, v15, v207
	v_lshlrev_b32_e32 v206, 16, v46
	v_and_b32_e32 v207, 0xffff0000, v46
	v_fmac_f32_e32 v208, v8, v206
	v_fmac_f32_e32 v209, v8, v207
	v_lshlrev_b32_e32 v206, 16, v54
	v_and_b32_e32 v207, 0xffff0000, v54
	v_fmac_f32_e32 v208, v9, v206
	v_fmac_f32_e32 v209, v9, v207
	v_lshlrev_b32_e32 v206, 16, v62
	v_and_b32_e32 v207, 0xffff0000, v62
	v_fmac_f32_e32 v208, v10, v206
	v_fmac_f32_e32 v209, v10, v207
	v_lshlrev_b32_e32 v206, 16, v70
	v_and_b32_e32 v207, 0xffff0000, v70
	v_fmac_f32_e32 v208, v11, v206
	v_fmac_f32_e32 v209, v11, v207
	v_cvt_pk_bf16_f32 v250, v208, v209
	v_lshlrev_b32_e32 v206, 16, v7
	v_and_b32_e32 v207, 0xffff0000, v7
	v_mul_f32_e32 v208, v12, v206
	v_mul_f32_e32 v209, v12, v207
	v_lshlrev_b32_e32 v206, 16, v23
	v_and_b32_e32 v207, 0xffff0000, v23
	v_fmac_f32_e32 v208, v13, v206
	v_fmac_f32_e32 v209, v13, v207
	v_lshlrev_b32_e32 v206, 16, v31
	v_and_b32_e32 v207, 0xffff0000, v31
	v_fmac_f32_e32 v208, v14, v206
	v_fmac_f32_e32 v209, v14, v207
	v_lshlrev_b32_e32 v206, 16, v39
	v_and_b32_e32 v207, 0xffff0000, v39
	v_fmac_f32_e32 v208, v15, v206
	v_fmac_f32_e32 v209, v15, v207
	v_lshlrev_b32_e32 v206, 16, v47
	v_and_b32_e32 v207, 0xffff0000, v47
	v_fmac_f32_e32 v208, v8, v206
	v_fmac_f32_e32 v209, v8, v207
	v_lshlrev_b32_e32 v206, 16, v55
	v_and_b32_e32 v207, 0xffff0000, v55
	v_fmac_f32_e32 v208, v9, v206
	v_fmac_f32_e32 v209, v9, v207
	v_lshlrev_b32_e32 v206, 16, v63
	v_and_b32_e32 v207, 0xffff0000, v63
	v_fmac_f32_e32 v208, v10, v206
	v_fmac_f32_e32 v209, v10, v207
	v_lshlrev_b32_e32 v206, 16, v71
	v_and_b32_e32 v207, 0xffff0000, v71
	v_fmac_f32_e32 v208, v11, v206
	v_fmac_f32_e32 v209, v11, v207
	v_cvt_pk_bf16_f32 v251, v208, v209
	s_barrier
	ds_write_b128 v122, v[74:77]
	ds_write_b128 v122, v[74:77] offset:8192
	ds_write_b128 v122, v[74:77] offset:16384
	ds_write_b128 v122, v[74:77] offset:24576
	ds_write_b128 v122, v[74:77] offset:32768
	ds_write_b128 v122, v[74:77] offset:40960
	ds_write_b128 v122, v[74:77] offset:49152
	ds_write_b128 v122, v[74:77] offset:57344
	s_and_saveexec_b64 s[14:15], vcc
	v_lshl_add_u32 v72, v72, 2, s3
	ds_write_b32 v72, v177 offset:192
	s_or_b64 exec, exec, s[14:15]
	s_lshl_b32 s83, s30, 5
	v_or_b32_e32 v72, s83, v125
	v_lshrrev_b32_e32 v127, 4, v126
	v_ashrrev_i32_e32 v73, 31, v72
	v_lshlrev_b32_e32 v74, 3, v127
	v_mul_u32_u24_e32 v229, 0x70, v125
	v_lshlrev_b64 v[72:73], 7, v[72:73]
	v_sub_u32_e32 v72, v72, v229
	v_lshl_add_u64 v[72:73], s[22:23], 0, v[72:73]
	v_lshlrev_b32_e32 v176, 5, v74
	v_lshl_add_u64 v[72:73], v[72:73], 0, v[176:177]
	s_waitcnt lgkmcnt(0)
	s_barrier
	global_load_dwordx4 v[100:103], v[72:73], off
	global_load_dwordx4 v[96:99], v[72:73], off offset:1024
	global_load_dwordx4 v[92:95], v[72:73], off offset:2048
	global_load_dwordx4 v[88:91], v[72:73], off offset:3072
	s_cmp_lt_i32 s30, s82
	v_lshl_add_u32 v128, v125, 12, 0
	s_cselect_b64 s[36:37], -1, 0
	s_cmp_ge_i32 s30, s82
	v_lshl_add_u64 v[120:121], s[22:23], 0, v[176:177]
	s_cbranch_scc1 .LBB0_1310
	s_waitcnt vmcnt(0)
	v_mov_b64_e32 v[106:107], v[90:91]
	s_add_i32 s14, s82, -1
	s_mov_b32 s15, s30
	v_mov_b64_e32 v[104:105], v[88:89]
	v_mov_b32_e32 v116, v100
	v_mov_b32_e32 v117, v101
	v_mov_b32_e32 v118, v102
	v_mov_b32_e32 v119, v103
	v_mov_b32_e32 v108, v96
	v_mov_b32_e32 v109, v97
	v_mov_b32_e32 v110, v98
	v_mov_b32_e32 v111, v99
	v_mov_b32_e32 v112, v92
	v_mov_b32_e32 v113, v93
	v_mov_b32_e32 v114, v94
	v_mov_b32_e32 v115, v95
	s_mul_i32 s32, s100, 0x600
	v_add_u32_e32 v232, s32, v230
	v_add_u32_e32 v223, s32, v197
	v_mov_b32_e32 v168, 0x05030201
	v_mov_b32_e32 v169, 0x06050302
	v_mov_b32_e32 v170, 0x07060503
	s_branch .LBB0_1308

.LBB0_1308:
	s_waitcnt vmcnt(5)
	v_mfma_f32_16x16x32_bf16 v[130:133], v[116:119], v[0:3], 0
	v_mfma_f32_16x16x32_bf16 v[156:159], v[116:119], v[244:247], 0
	s_min_i32 s32, s15, s100
	s_mul_i32 s32, s32, 0x600
	v_add_u32_e32 v231, s32, v230
	v_add_u32_e32 v222, s32, v197
	s_add_i32 s31, s15, 8
	s_min_i32 s35, s31, s14
	v_lshl_or_b32 v72, s35, 5, v125
	s_waitcnt vmcnt(3)
	v_mfma_f32_16x16x32_bf16 v[134:137], v[112:115], v[0:3], 0
	v_mfma_f32_16x16x32_bf16 v[160:163], v[112:115], v[244:247], 0
	v_ashrrev_i32_e32 v73, 31, v72
	v_lshlrev_b64 v[72:73], 7, v[72:73]
	v_sub_u32_e32 v72, v72, v229
	v_lshl_add_u64 v[84:85], v[120:121], 0, v[72:73]
	v_mfma_f32_16x16x32_bf16 v[138:141], v[108:111], v[4:7], v[130:133]
	v_mfma_f32_16x16x32_bf16 v[156:159], v[108:111], v[248:251], v[156:159]
	global_load_dwordx4 v[72:75], v[84:85], off
	global_load_dwordx4 v[76:79], v[84:85], off offset:1024
	global_load_dwordx4 v[80:83], v[84:85], off offset:2048
	s_nop 0
	global_load_dwordx4 v[84:87], v[84:85], off offset:3072
	global_store_dwordx4 v232, v[216:219], s[20:21]
	global_store_dwordx2 v223, v[220:221], s[20:21]
	s_nop 1
	s_nop 0
	s_add_i32 s15, s15, 16
	s_waitcnt vmcnt(8)
	v_mfma_f32_16x16x32_bf16 v[132:135], v[104:107], v[4:7], v[134:137]
	v_mfma_f32_16x16x32_bf16 v[160:163], v[104:107], v[248:251], v[160:163]
	s_min_i32 s35, s15, s14
	s_cmp_ge_i32 s31, s82
	v_mfma_f32_16x16x32_bf16 v[142:145], v[116:119], v[16:19], 0
	v_mfma_f32_16x16x32_bf16 v[146:149], v[112:115], v[16:19], 0
	v_mfma_f32_16x16x32_bf16 v[142:145], v[108:111], v[20:23], v[142:145]
	v_mfma_f32_16x16x32_bf16 v[146:149], v[104:107], v[20:23], v[146:149]
	s_nop 3
	v_fma_f32 v156, v12, |v138|, v156
	v_fma_f32 v160, v12, |v132|, v160
	v_fma_f32 v157, v12, |v139|, v157
	v_fma_f32 v161, v12, |v133|, v161
	v_fma_f32 v158, v12, |v140|, v158
	v_fma_f32 v162, v12, |v134|, v162
	v_fma_f32 v159, v12, |v141|, v159
	v_fma_f32 v163, v12, |v135|, v163
	v_mfma_f32_16x16x32_bf16 v[138:141], v[116:119], v[24:27], 0
	v_mfma_f32_16x16x32_bf16 v[132:135], v[112:115], v[24:27], 0
	v_mfma_f32_16x16x32_bf16 v[138:141], v[108:111], v[28:31], v[138:141]
	v_mfma_f32_16x16x32_bf16 v[132:135], v[104:107], v[28:31], v[132:135]
	s_nop 3
	v_fma_f32 v156, v13, |v142|, v156
	v_fma_f32 v160, v13, |v146|, v160
	v_fma_f32 v157, v13, |v143|, v157
	v_fma_f32 v161, v13, |v147|, v161
	v_fma_f32 v158, v13, |v144|, v158
	v_fma_f32 v162, v13, |v148|, v162
	v_fma_f32 v159, v13, |v145|, v159
	v_fma_f32 v163, v13, |v149|, v163
	v_mfma_f32_16x16x32_bf16 v[142:145], v[116:119], v[32:35], 0
	v_mfma_f32_16x16x32_bf16 v[146:149], v[112:115], v[32:35], 0
	v_mfma_f32_16x16x32_bf16 v[142:145], v[108:111], v[36:39], v[142:145]
	v_mfma_f32_16x16x32_bf16 v[146:149], v[104:107], v[36:39], v[146:149]
	s_nop 3
	v_fma_f32 v156, v14, |v138|, v156
	v_fma_f32 v160, v14, |v132|, v160
	v_fma_f32 v157, v14, |v139|, v157
	v_fma_f32 v161, v14, |v133|, v161
	v_fma_f32 v158, v14, |v140|, v158
	v_fma_f32 v162, v14, |v134|, v162
	v_fma_f32 v159, v14, |v141|, v159
	v_fma_f32 v163, v14, |v135|, v163
	v_mfma_f32_16x16x32_bf16 v[138:141], v[116:119], v[40:43], 0
	v_mfma_f32_16x16x32_bf16 v[132:135], v[112:115], v[40:43], 0
	v_mfma_f32_16x16x32_bf16 v[138:141], v[108:111], v[44:47], v[138:141]
	v_mfma_f32_16x16x32_bf16 v[132:135], v[104:107], v[44:47], v[132:135]
	s_nop 3
	v_fma_f32 v156, v15, |v142|, v156
	v_fma_f32 v160, v15, |v146|, v160
	v_fma_f32 v157, v15, |v143|, v157
	v_fma_f32 v161, v15, |v147|, v161
	v_fma_f32 v158, v15, |v144|, v158
	v_fma_f32 v162, v15, |v148|, v162
	v_fma_f32 v159, v15, |v145|, v159
	v_fma_f32 v163, v15, |v149|, v163
	v_mfma_f32_16x16x32_bf16 v[142:145], v[116:119], v[48:51], 0
	v_mfma_f32_16x16x32_bf16 v[146:149], v[112:115], v[48:51], 0
	v_mfma_f32_16x16x32_bf16 v[142:145], v[108:111], v[52:55], v[142:145]
	v_mfma_f32_16x16x32_bf16 v[146:149], v[104:107], v[52:55], v[146:149]
	s_nop 3
	v_fma_f32 v156, v8, |v138|, v156
	v_fma_f32 v160, v8, |v132|, v160
	v_fma_f32 v157, v8, |v139|, v157
	v_fma_f32 v161, v8, |v133|, v161
	v_fma_f32 v158, v8, |v140|, v158
	v_fma_f32 v162, v8, |v134|, v162
	v_fma_f32 v159, v8, |v141|, v159
	v_fma_f32 v163, v8, |v135|, v163
	v_mfma_f32_16x16x32_bf16 v[138:141], v[116:119], v[56:59], 0
	v_mfma_f32_16x16x32_bf16 v[132:135], v[112:115], v[56:59], 0
	v_mfma_f32_16x16x32_bf16 v[138:141], v[108:111], v[60:63], v[138:141]
	v_mfma_f32_16x16x32_bf16 v[132:135], v[104:107], v[60:63], v[132:135]
	s_nop 3
	v_fma_f32 v156, v9, |v142|, v156
	v_fma_f32 v160, v9, |v146|, v160
	v_fma_f32 v157, v9, |v143|, v157
	v_fma_f32 v161, v9, |v147|, v161
	v_fma_f32 v158, v9, |v144|, v158
	v_fma_f32 v162, v9, |v148|, v162
	v_fma_f32 v159, v9, |v145|, v159
	v_fma_f32 v163, v9, |v149|, v163
	v_mfma_f32_16x16x32_bf16 v[142:145], v[116:119], v[64:67], 0
	v_mfma_f32_16x16x32_bf16 v[146:149], v[112:115], v[64:67], 0
	v_mfma_f32_16x16x32_bf16 v[142:145], v[108:111], v[68:71], v[142:145]
	v_mfma_f32_16x16x32_bf16 v[146:149], v[104:107], v[68:71], v[146:149]
	s_nop 3
	v_fma_f32 v156, v10, |v138|, v156
	v_fma_f32 v160, v10, |v132|, v160
	v_fma_f32 v157, v10, |v139|, v157
	v_fma_f32 v161, v10, |v133|, v161
	v_fma_f32 v158, v10, |v140|, v158
	v_fma_f32 v162, v10, |v134|, v162
	v_fma_f32 v159, v10, |v141|, v159
	v_fma_f32 v163, v10, |v135|, v163
	s_nop 7
	v_fma_f32 v156, v11, |v142|, v156
	v_fma_f32 v160, v11, |v146|, v160
	v_fma_f32 v157, v11, |v143|, v157
	v_fma_f32 v161, v11, |v147|, v161
	v_fma_f32 v158, v11, |v144|, v158
	v_fma_f32 v162, v11, |v148|, v162
	v_fma_f32 v159, v11, |v145|, v159
	v_fma_f32 v163, v11, |v149|, v163
	s_nop 0
	v_lshrrev_b32 v104, 22, v156
	v_bfe_u32 v105, v156, 21, 1
	v_lshl_add_u32 v104, v104, 2, v128
	v_mad_u32_u24 v105, v105, s1, 1
	ds_add_u32 v104, v105
	v_lshrrev_b32 v104, 22, v157
	v_bfe_u32 v105, v157, 21, 1
	v_lshl_add_u32 v104, v104, 2, v128
	v_mad_u32_u24 v105, v105, s1, 1
	ds_add_u32 v104, v105
	v_lshrrev_b32 v104, 22, v158
	v_bfe_u32 v105, v158, 21, 1
	v_lshl_add_u32 v104, v104, 2, v128
	v_mad_u32_u24 v105, v105, s1, 1
	ds_add_u32 v104, v105
	v_lshrrev_b32 v104, 22, v159
	v_bfe_u32 v105, v159, 21, 1
	v_lshl_add_u32 v104, v104, 2, v128
	v_mad_u32_u24 v105, v105, s1, 1
	ds_add_u32 v104, v105
	v_lshrrev_b32 v104, 22, v160
	v_bfe_u32 v105, v160, 21, 1
	v_lshl_add_u32 v104, v104, 2, v128
	v_mad_u32_u24 v105, v105, s1, 1
	ds_add_u32 v104, v105
	v_lshrrev_b32 v104, 22, v161
	v_bfe_u32 v105, v161, 21, 1
	v_lshl_add_u32 v104, v104, 2, v128
	v_mad_u32_u24 v105, v105, s1, 1
	ds_add_u32 v104, v105
	v_lshrrev_b32 v104, 22, v162
	v_bfe_u32 v105, v162, 21, 1
	v_lshl_add_u32 v104, v104, 2, v128
	v_mad_u32_u24 v105, v105, s1, 1
	ds_add_u32 v104, v105
	v_lshrrev_b32 v104, 22, v163
	v_bfe_u32 v105, v163, 21, 1
	v_lshl_add_u32 v104, v104, 2, v128
	v_mad_u32_u24 v105, v105, s1, 1
	ds_add_u32 v104, v105
	v_lshl_or_b32 v104, s35, 5, v125
	v_ashrrev_i32_e32 v105, 31, v104
	v_lshlrev_b64 v[104:105], 7, v[104:105]
	v_sub_u32_e32 v104, v104, v229
	v_lshl_add_u64 v[104:105], v[120:121], 0, v[104:105]
	global_load_dwordx4 v[116:119], v[104:105], off
	global_load_dwordx4 v[108:111], v[104:105], off offset:1024
	global_load_dwordx4 v[112:115], v[104:105], off offset:2048
	s_nop 0
	global_load_dwordx4 v[104:107], v[104:105], off offset:3072
	v_perm_b32 v208, v157, v156, v168
	v_perm_b32 v209, v158, v157, v169
	v_perm_b32 v210, v159, v158, v170
	v_perm_b32 v211, v161, v160, v168
	v_perm_b32 v212, v162, v161, v169
	v_perm_b32 v213, v163, v162, v170
	global_store_dwordx4 v231, v[208:211], s[20:21]
	global_store_dwordx2 v222, v[212:213], s[20:21]
	s_cbranch_scc1 .LBB0_1307
	s_waitcnt vmcnt(11)
	v_mfma_f32_16x16x32_bf16 v[130:133], v[72:75], v[0:3], 0
	v_mfma_f32_16x16x32_bf16 v[164:167], v[72:75], v[244:247], 0
	s_min_i32 s32, s31, s100
	s_mul_i32 s32, s32, 0x600
	v_add_u32_e32 v232, s32, v230
	v_add_u32_e32 v223, s32, v197
	s_waitcnt vmcnt(9)
	v_mfma_f32_16x16x32_bf16 v[134:137], v[80:83], v[0:3], 0
	v_mfma_f32_16x16x32_bf16 v[186:189], v[80:83], v[244:247], 0
	v_mfma_f32_16x16x32_bf16 v[138:141], v[76:79], v[4:7], v[130:133]
	v_mfma_f32_16x16x32_bf16 v[164:167], v[76:79], v[248:251], v[164:167]
	s_waitcnt vmcnt(8)
	v_mfma_f32_16x16x32_bf16 v[132:135], v[84:87], v[4:7], v[134:137]
	v_mfma_f32_16x16x32_bf16 v[186:189], v[84:87], v[248:251], v[186:189]
	v_mfma_f32_16x16x32_bf16 v[142:145], v[72:75], v[16:19], 0
	v_mfma_f32_16x16x32_bf16 v[146:149], v[80:83], v[16:19], 0
	v_mfma_f32_16x16x32_bf16 v[142:145], v[76:79], v[20:23], v[142:145]
	v_mfma_f32_16x16x32_bf16 v[146:149], v[84:87], v[20:23], v[146:149]
	s_nop 3
	v_fma_f32 v164, v12, |v138|, v164
	v_fma_f32 v186, v12, |v132|, v186
	v_fma_f32 v165, v12, |v139|, v165
	v_fma_f32 v187, v12, |v133|, v187
	v_fma_f32 v166, v12, |v140|, v166
	v_fma_f32 v188, v12, |v134|, v188
	v_fma_f32 v167, v12, |v141|, v167
	v_fma_f32 v189, v12, |v135|, v189
	v_mfma_f32_16x16x32_bf16 v[138:141], v[72:75], v[24:27], 0
	v_mfma_f32_16x16x32_bf16 v[132:135], v[80:83], v[24:27], 0
	v_mfma_f32_16x16x32_bf16 v[138:141], v[76:79], v[28:31], v[138:141]
	v_mfma_f32_16x16x32_bf16 v[132:135], v[84:87], v[28:31], v[132:135]
	s_nop 3
	v_fma_f32 v164, v13, |v142|, v164
	v_fma_f32 v186, v13, |v146|, v186
	v_fma_f32 v165, v13, |v143|, v165
	v_fma_f32 v187, v13, |v147|, v187
	v_fma_f32 v166, v13, |v144|, v166
	v_fma_f32 v188, v13, |v148|, v188
	v_fma_f32 v167, v13, |v145|, v167
	v_fma_f32 v189, v13, |v149|, v189
	v_mfma_f32_16x16x32_bf16 v[142:145], v[72:75], v[32:35], 0
	v_mfma_f32_16x16x32_bf16 v[146:149], v[80:83], v[32:35], 0
	v_mfma_f32_16x16x32_bf16 v[142:145], v[76:79], v[36:39], v[142:145]
	v_mfma_f32_16x16x32_bf16 v[146:149], v[84:87], v[36:39], v[146:149]
	s_nop 3
	v_fma_f32 v164, v14, |v138|, v164
	v_fma_f32 v186, v14, |v132|, v186
	v_fma_f32 v165, v14, |v139|, v165
	v_fma_f32 v187, v14, |v133|, v187
	v_fma_f32 v166, v14, |v140|, v166
	v_fma_f32 v188, v14, |v134|, v188
	v_fma_f32 v167, v14, |v141|, v167
	v_fma_f32 v189, v14, |v135|, v189
	v_mfma_f32_16x16x32_bf16 v[138:141], v[72:75], v[40:43], 0
	v_mfma_f32_16x16x32_bf16 v[132:135], v[80:83], v[40:43], 0
	v_mfma_f32_16x16x32_bf16 v[138:141], v[76:79], v[44:47], v[138:141]
	v_mfma_f32_16x16x32_bf16 v[132:135], v[84:87], v[44:47], v[132:135]
	s_nop 3
	v_fma_f32 v164, v15, |v142|, v164
	v_fma_f32 v186, v15, |v146|, v186
	v_fma_f32 v165, v15, |v143|, v165
	v_fma_f32 v187, v15, |v147|, v187
	v_fma_f32 v166, v15, |v144|, v166
	v_fma_f32 v188, v15, |v148|, v188
	v_fma_f32 v167, v15, |v145|, v167
	v_fma_f32 v189, v15, |v149|, v189
	v_mfma_f32_16x16x32_bf16 v[142:145], v[72:75], v[48:51], 0
	v_mfma_f32_16x16x32_bf16 v[146:149], v[80:83], v[48:51], 0
	v_mfma_f32_16x16x32_bf16 v[142:145], v[76:79], v[52:55], v[142:145]
	v_mfma_f32_16x16x32_bf16 v[146:149], v[84:87], v[52:55], v[146:149]
	s_nop 3
	v_fma_f32 v164, v8, |v138|, v164
	v_fma_f32 v186, v8, |v132|, v186
	v_fma_f32 v165, v8, |v139|, v165
	v_fma_f32 v187, v8, |v133|, v187
	v_fma_f32 v166, v8, |v140|, v166
	v_fma_f32 v188, v8, |v134|, v188
	v_fma_f32 v167, v8, |v141|, v167
	v_fma_f32 v189, v8, |v135|, v189
	v_mfma_f32_16x16x32_bf16 v[138:141], v[72:75], v[56:59], 0
	v_mfma_f32_16x16x32_bf16 v[132:135], v[80:83], v[56:59], 0
	v_mfma_f32_16x16x32_bf16 v[138:141], v[76:79], v[60:63], v[138:141]
	v_mfma_f32_16x16x32_bf16 v[132:135], v[84:87], v[60:63], v[132:135]
	s_nop 3
	v_fma_f32 v164, v9, |v142|, v164
	v_fma_f32 v186, v9, |v146|, v186
	v_fma_f32 v165, v9, |v143|, v165
	v_fma_f32 v187, v9, |v147|, v187
	v_fma_f32 v166, v9, |v144|, v166
	v_fma_f32 v188, v9, |v148|, v188
	v_fma_f32 v167, v9, |v145|, v167
	v_fma_f32 v189, v9, |v149|, v189
	v_mfma_f32_16x16x32_bf16 v[142:145], v[72:75], v[64:67], 0
	v_mfma_f32_16x16x32_bf16 v[146:149], v[80:83], v[64:67], 0
	v_mfma_f32_16x16x32_bf16 v[142:145], v[76:79], v[68:71], v[142:145]
	v_mfma_f32_16x16x32_bf16 v[146:149], v[84:87], v[68:71], v[146:149]
	s_nop 3
	v_fma_f32 v164, v10, |v138|, v164
	v_fma_f32 v186, v10, |v132|, v186
	v_fma_f32 v165, v10, |v139|, v165
	v_fma_f32 v187, v10, |v133|, v187
	v_fma_f32 v166, v10, |v140|, v166
	v_fma_f32 v188, v10, |v134|, v188
	v_fma_f32 v167, v10, |v141|, v167
	v_fma_f32 v189, v10, |v135|, v189
	s_nop 7
	v_fma_f32 v164, v11, |v142|, v164
	v_fma_f32 v186, v11, |v146|, v186
	v_fma_f32 v165, v11, |v143|, v165
	v_fma_f32 v187, v11, |v147|, v187
	v_fma_f32 v166, v11, |v144|, v166
	v_fma_f32 v188, v11, |v148|, v188
	v_fma_f32 v167, v11, |v145|, v167
	v_fma_f32 v189, v11, |v149|, v189
	v_lshrrev_b32 v135, 22, v164
	v_bfe_u32 v131, v164, 21, 1
	v_mad_u32_u24 v131, v131, s1, 1
	v_lshl_add_u32 v135, v135, 2, v128
	ds_add_u32 v135, v131
	v_lshrrev_b32 v131, 22, v165
	v_bfe_u32 v132, v165, 21, 1
	v_lshl_add_u32 v131, v131, 2, v128
	v_mad_u32_u24 v132, v132, s1, 1
	ds_add_u32 v131, v132
	v_lshrrev_b32 v131, 22, v166
	v_bfe_u32 v132, v166, 21, 1
	v_lshl_add_u32 v131, v131, 2, v128
	v_mad_u32_u24 v132, v132, s1, 1
	ds_add_u32 v131, v132
	v_lshrrev_b32 v131, 22, v167
	v_bfe_u32 v132, v167, 21, 1
	v_lshl_add_u32 v131, v131, 2, v128
	v_mad_u32_u24 v132, v132, s1, 1
	ds_add_u32 v131, v132
	v_lshrrev_b32 v131, 22, v186
	v_bfe_u32 v123, v186, 21, 1
	v_mad_u32_u24 v123, v123, s1, 1
	v_lshl_add_u32 v131, v131, 2, v128
	ds_add_u32 v131, v123
	v_lshrrev_b32 v123, 22, v187
	v_bfe_u32 v124, v187, 21, 1
	v_lshl_add_u32 v123, v123, 2, v128
	v_mad_u32_u24 v124, v124, s1, 1
	ds_add_u32 v123, v124
	v_lshrrev_b32 v123, 22, v188
	v_bfe_u32 v124, v188, 21, 1
	v_lshl_add_u32 v123, v123, 2, v128
	v_mad_u32_u24 v124, v124, s1, 1
	ds_add_u32 v123, v124
	v_lshrrev_b32 v123, 22, v189
	v_bfe_u32 v124, v189, 21, 1
	v_lshl_add_u32 v123, v123, 2, v128
	v_mad_u32_u24 v124, v124, s1, 1
	ds_add_u32 v123, v124
	v_perm_b32 v216, v165, v164, v168
	v_perm_b32 v217, v166, v165, v169
	v_perm_b32 v218, v167, v166, v170
	v_perm_b32 v219, v187, v186, v168
	v_perm_b32 v220, v188, v187, v169
	v_perm_b32 v221, v189, v188, v170
	s_cmp_ge_i32 s15, s82
	s_cbranch_scc0 .LBB0_1308
	global_store_dwordx4 v232, v[216:219], s[20:21]
	global_store_dwordx2 v223, v[220:221], s[20:21]
	s_branch .LBB0_1310

.Lpb2_entry:
	s_waitcnt vmcnt(0)
	s_min_i32 s32, s82, s100
	v_mov_b32_e32 v235, 0xffff
	v_ashrrev_i32_e32 v196, 31, v139
	v_mov_b32_e32 v155, 0x0201000c
	v_mov_b32_e32 v168, 0x0504030c
	v_mov_b32_e32 v169, 0x0403020c
	v_mov_b32_e32 v170, 0x0302010c
	s_mul_i32 s85, s100, 0x600
	v_add_u32_e32 v234, s85, v230
	s_add_i32 s85, s31, 0
	s_min_i32 s85, s85, s100
	s_mul_i32 s85, s85, 0x600
	v_add_u32_e32 v233, s85, v230
	v_add_u32_e32 v226, s85, v197
	global_load_dwordx4 v[156:159], v233, s[20:21]
	global_load_dwordx2 v[160:161], v226, s[20:21]
	global_store_dword v234, v193, s[20:21]
	s_add_i32 s85, s31, 8
	s_min_i32 s85, s85, s100
	s_mul_i32 s85, s85, 0x600
	v_add_u32_e32 v233, s85, v230
	v_add_u32_e32 v226, s85, v197
	global_load_dwordx4 v[178:181], v233, s[20:21]
	global_load_dwordx2 v[182:183], v226, s[20:21]
	global_store_dword v234, v193, s[20:21]
	s_add_i32 s85, s31, 16
	s_min_i32 s85, s85, s100
	s_mul_i32 s85, s85, 0x600
	v_add_u32_e32 v233, s85, v230
	v_add_u32_e32 v226, s85, v197
	global_load_dwordx4 v[236:239], v233, s[20:21]
	global_load_dwordx2 v[240:241], v226, s[20:21]
	global_store_dword v234, v193, s[20:21]
	s_add_i32 s85, s31, 24
	s_min_i32 s85, s85, s100
	s_mul_i32 s85, s85, 0x600
	v_add_u32_e32 v233, s85, v230
	v_add_u32_e32 v226, s85, v197
	global_load_dwordx4 v[80:83], v233, s[20:21]
	global_load_dwordx2 v[84:85], v226, s[20:21]
	global_store_dword v234, v193, s[20:21]
.Lpb2_i0:
	s_add_i32 s85, s31, 32
	s_min_i32 s85, s85, s100
	s_mul_i32 s85, s85, 0x600
	v_add_u32_e32 v233, s85, v230
	v_add_u32_e32 v226, s85, v197
	global_load_dwordx4 v[72:75], v233, s[20:21]
	global_load_dwordx2 v[76:77], v226, s[20:21]
	s_waitcnt vmcnt(12)
	v_perm_b32 v164, v156, v156, v155
	v_perm_b32 v165, v157, v156, v168
	v_perm_b32 v166, v158, v157, v169
	v_perm_b32 v167, v158, v158, v170
	v_perm_b32 v186, v159, v159, v155
	v_perm_b32 v187, v160, v159, v168
	v_perm_b32 v188, v161, v160, v169
	v_perm_b32 v189, v161, v161, v170
	v_cmp_ge_f32_e64 s[66:67], v164, v140
	v_cmp_ge_f32_e64 s[50:51], v164, v139
	v_cmp_ge_f32_e32 vcc, v165, v140
	v_cmp_ge_f32_e64 s[52:53], v165, v139
	v_cndmask_b32_e64 v224, 0, 1, s[66:67]
	v_cndmask_b32_e64 v225, 0, 2, vcc
	s_andn2_b64 s[50:51], s[50:51], s[66:67]
	s_andn2_b64 s[52:53], s[52:53], vcc
	v_or_b32_e32 v228, v224, v225
	v_cmp_ge_f32_e64 s[66:67], v166, v140
	v_cmp_ge_f32_e64 s[54:55], v166, v139
	v_cmp_ge_f32_e32 vcc, v167, v140
	v_cmp_ge_f32_e64 s[56:57], v167, v139
	v_cndmask_b32_e64 v224, 0, 4, s[66:67]
	v_cndmask_b32_e64 v225, 0, 8, vcc
	s_andn2_b64 s[54:55], s[54:55], s[66:67]
	s_andn2_b64 s[56:57], s[56:57], vcc
	v_or3_b32 v228, v228, v224, v225
	v_cmp_ge_f32_e64 s[66:67], v186, v140
	v_cmp_ge_f32_e64 s[58:59], v186, v139
	v_cmp_ge_f32_e32 vcc, v187, v140
	v_cmp_ge_f32_e64 s[60:61], v187, v139
	v_cndmask_b32_e64 v224, 0, v201, s[66:67]
	v_cndmask_b32_e64 v225, 0, v200, vcc
	s_andn2_b64 s[58:59], s[58:59], s[66:67]
	s_andn2_b64 s[60:61], s[60:61], vcc
	v_or3_b32 v228, v228, v224, v225
	v_cmp_ge_f32_e64 s[66:67], v188, v140
	v_cmp_ge_f32_e64 s[62:63], v188, v139
	v_cmp_ge_f32_e32 vcc, v189, v140
	v_cmp_ge_f32_e64 s[64:65], v189, v139
	v_cndmask_b32_e64 v224, 0, v199, s[66:67]
	v_cndmask_b32_e64 v225, 0, v198, vcc
	s_andn2_b64 s[62:63], s[62:63], s[66:67]
	s_andn2_b64 s[64:65], s[64:65], vcc
	v_or3_b32 v228, v228, v224, v225
	v_lshlrev_b32_e32 v104, v143, v228
	ds_bpermute_b32 v105, v144, v104
	v_mov_b32_e32 v227, s96
	s_mov_b64 s[14:15], exec
	s_mov_b64 exec, s[50:51]
	ds_add_rtn_u32 v214, v142, v193
	s_mov_b64 exec, s[52:53]
	ds_add_rtn_u32 v215, v142, v193
	s_mov_b64 exec, s[54:55]
	ds_add_rtn_u32 v216, v142, v193
	s_mov_b64 exec, s[56:57]
	ds_add_rtn_u32 v217, v142, v193
	s_mov_b64 exec, s[58:59]
	ds_add_rtn_u32 v218, v142, v193
	s_mov_b64 exec, s[60:61]
	ds_add_rtn_u32 v219, v142, v193
	s_mov_b64 exec, s[62:63]
	ds_add_rtn_u32 v220, v142, v193
	s_mov_b64 exec, s[64:65]
	ds_add_rtn_u32 v221, v142, v193
	s_mov_b64 exec, s[50:51]
	v_xor_b32_e32 v206, v196, v164
	v_bfe_u32 v222, v206, 11, 10
	v_bfe_u32 v223, v206, 10, 1
	v_lshl_add_u32 v222, v222, 2, v128
	v_mad_u32_u24 v223, v223, v235, 1
	ds_add_u32 v222, v223
	s_mov_b64 exec, s[52:53]
	v_xor_b32_e32 v207, v196, v165
	v_bfe_u32 v222, v207, 11, 10
	v_bfe_u32 v223, v207, 10, 1
	v_lshl_add_u32 v222, v222, 2, v128
	v_mad_u32_u24 v223, v223, v235, 1
	ds_add_u32 v222, v223
	s_mov_b64 exec, s[54:55]
	v_xor_b32_e32 v208, v196, v166
	v_bfe_u32 v222, v208, 11, 10
	v_bfe_u32 v223, v208, 10, 1
	v_lshl_add_u32 v222, v222, 2, v128
	v_mad_u32_u24 v223, v223, v235, 1
	ds_add_u32 v222, v223
	s_mov_b64 exec, s[56:57]
	v_xor_b32_e32 v209, v196, v167
	v_bfe_u32 v222, v209, 11, 10
	v_bfe_u32 v223, v209, 10, 1
	v_lshl_add_u32 v222, v222, 2, v128
	v_mad_u32_u24 v223, v223, v235, 1
	ds_add_u32 v222, v223
	s_waitcnt lgkmcnt(8)
	s_mov_b64 exec, s[58:59]
	v_xor_b32_e32 v210, v196, v186
	v_bfe_u32 v222, v210, 11, 10
	v_bfe_u32 v223, v210, 10, 1
	v_lshl_add_u32 v222, v222, 2, v128
	v_mad_u32_u24 v223, v223, v235, 1
	ds_add_u32 v222, v223
	s_mov_b64 exec, s[60:61]
	v_xor_b32_e32 v211, v196, v187
	v_bfe_u32 v222, v211, 11, 10
	v_bfe_u32 v223, v211, 10, 1
	v_lshl_add_u32 v222, v222, 2, v128
	v_mad_u32_u24 v223, v223, v235, 1
	ds_add_u32 v222, v223
	s_mov_b64 exec, s[62:63]
	v_xor_b32_e32 v212, v196, v188
	v_bfe_u32 v222, v212, 11, 10
	v_bfe_u32 v223, v212, 10, 1
	v_lshl_add_u32 v222, v222, 2, v128
	v_mad_u32_u24 v223, v223, v235, 1
	ds_add_u32 v222, v223
	s_mov_b64 exec, s[64:65]
	v_xor_b32_e32 v213, v196, v189
	v_bfe_u32 v222, v213, 11, 10
	v_bfe_u32 v223, v213, 10, 1
	v_lshl_add_u32 v222, v222, 2, v128
	v_mad_u32_u24 v223, v223, v235, 1
	ds_add_u32 v222, v223
	s_waitcnt lgkmcnt(8)
	s_mov_b64 exec, s[14:15]
	v_or_b32_e32 v104, v105, v104
	ds_bpermute_b32 v105, v145, v104
	s_mov_b64 exec, s[50:51]
	v_cmp_lt_u32_e64 s[66:67], s0, v214
	s_add_i32 s85, s74, 0x0
	v_bfe_u32 v224, v206, 10, 11
	v_lshl_add_u32 v222, v214, 2, v141
	v_add3_u32 v224, v224, v124, s85
	s_andn2_b64 exec, exec, s[66:67]
	ds_write_b32 v222, v224
	s_mov_b64 exec, s[66:67]
	ds_write_b32 v227, v193
	s_mov_b64 exec, s[52:53]
	v_cmp_lt_u32_e64 s[66:67], s0, v215
	s_add_i32 s85, s74, 0x800
	v_bfe_u32 v224, v207, 10, 11
	v_lshl_add_u32 v222, v215, 2, v141
	v_add3_u32 v224, v224, v124, s85
	s_andn2_b64 exec, exec, s[66:67]
	ds_write_b32 v222, v224
	s_mov_b64 exec, s[66:67]
	ds_write_b32 v227, v193
	s_waitcnt lgkmcnt(8)
	s_mov_b64 exec, s[54:55]
	v_cmp_lt_u32_e64 s[66:67], s0, v216
	s_add_i32 s85, s74, 0x1000
	v_bfe_u32 v224, v208, 10, 11
	v_lshl_add_u32 v222, v216, 2, v141
	v_add3_u32 v224, v224, v124, s85
	s_andn2_b64 exec, exec, s[66:67]
	ds_write_b32 v222, v224
	s_mov_b64 exec, s[66:67]
	ds_write_b32 v227, v193
	s_mov_b64 exec, s[56:57]
	v_cmp_lt_u32_e64 s[66:67], s0, v217
	s_add_i32 s85, s74, 0x1800
	v_bfe_u32 v224, v209, 10, 11
	v_lshl_add_u32 v222, v217, 2, v141
	v_add3_u32 v224, v224, v124, s85
	s_andn2_b64 exec, exec, s[66:67]
	ds_write_b32 v222, v224
	s_mov_b64 exec, s[66:67]
	ds_write_b32 v227, v193
	s_waitcnt lgkmcnt(8)
	s_mov_b64 exec, s[58:59]
	v_cmp_lt_u32_e64 s[66:67], s0, v218
	s_add_i32 s85, s74, 0x8000
	v_bfe_u32 v224, v210, 10, 11
	v_lshl_add_u32 v222, v218, 2, v141
	v_add3_u32 v224, v224, v124, s85
	s_andn2_b64 exec, exec, s[66:67]
	ds_write_b32 v222, v224
	s_mov_b64 exec, s[66:67]
	ds_write_b32 v227, v193
	s_mov_b64 exec, s[60:61]
	v_cmp_lt_u32_e64 s[66:67], s0, v219
	s_add_i32 s85, s74, 0x8800
	v_bfe_u32 v224, v211, 10, 11
	v_lshl_add_u32 v222, v219, 2, v141
	v_add3_u32 v224, v224, v124, s85
	s_andn2_b64 exec, exec, s[66:67]
	ds_write_b32 v222, v224
	s_mov_b64 exec, s[66:67]
	ds_write_b32 v227, v193
	s_waitcnt lgkmcnt(8)
	s_mov_b64 exec, s[62:63]
	v_cmp_lt_u32_e64 s[66:67], s0, v220
	s_add_i32 s85, s74, 0x9000
	v_bfe_u32 v224, v212, 10, 11
	v_lshl_add_u32 v222, v220, 2, v141
	v_add3_u32 v224, v224, v124, s85
	s_andn2_b64 exec, exec, s[66:67]
	ds_write_b32 v222, v224
	s_mov_b64 exec, s[66:67]
	ds_write_b32 v227, v193
	s_mov_b64 exec, s[64:65]
	v_cmp_lt_u32_e64 s[66:67], s0, v221
	s_add_i32 s85, s74, 0x9800
	v_bfe_u32 v224, v213, 10, 11
	v_lshl_add_u32 v222, v221, 2, v141
	v_add3_u32 v224, v224, v124, s85
	s_andn2_b64 exec, exec, s[66:67]
	ds_write_b32 v222, v224
	s_mov_b64 exec, s[66:67]
	ds_write_b32 v227, v193
	s_mov_b64 exec, s[14:15]
	s_and_saveexec_b64 s[14:15], s[38:39]
	v_or_b32_e32 v106, v104, v105
	v_lshl_add_u64 v[104:105], v[122:123], 0, s[74:75]
	v_add_co_u32_e32 v104, vcc, 0x3f700000, v104
	s_nop 1
	v_addc_co_u32_e32 v105, vcc, 0, v105, vcc
	global_store_dword v[104:105], v106, off
	s_or_b64 exec, exec, s[14:15]
	s_add_u32 s74, s74, 0x80000
	s_addc_u32 s75, s75, 0
	s_add_i32 s31, s31, 8
	s_cmp_ge_i32 s31, s32
	s_cbranch_scc1 .Lpb2_done
.Lpb2_i1:
	s_add_i32 s85, s31, 32
	s_min_i32 s85, s85, s100
	s_mul_i32 s85, s85, 0x600
	v_add_u32_e32 v233, s85, v230
	v_add_u32_e32 v226, s85, v197
	global_load_dwordx4 v[156:159], v233, s[20:21]
	global_load_dwordx2 v[160:161], v226, s[20:21]
	s_waitcnt vmcnt(12)
	v_perm_b32 v164, v178, v178, v155
	v_perm_b32 v165, v179, v178, v168
	v_perm_b32 v166, v180, v179, v169
	v_perm_b32 v167, v180, v180, v170
	v_perm_b32 v186, v181, v181, v155
	v_perm_b32 v187, v182, v181, v168
	v_perm_b32 v188, v183, v182, v169
	v_perm_b32 v189, v183, v183, v170
	v_cmp_ge_f32_e64 s[66:67], v164, v140
	v_cmp_ge_f32_e64 s[50:51], v164, v139
	v_cmp_ge_f32_e32 vcc, v165, v140
	v_cmp_ge_f32_e64 s[52:53], v165, v139
	v_cndmask_b32_e64 v224, 0, 1, s[66:67]
	v_cndmask_b32_e64 v225, 0, 2, vcc
	s_andn2_b64 s[50:51], s[50:51], s[66:67]
	s_andn2_b64 s[52:53], s[52:53], vcc
	v_or_b32_e32 v228, v224, v225
	v_cmp_ge_f32_e64 s[66:67], v166, v140
	v_cmp_ge_f32_e64 s[54:55], v166, v139
	v_cmp_ge_f32_e32 vcc, v167, v140
	v_cmp_ge_f32_e64 s[56:57], v167, v139
	v_cndmask_b32_e64 v224, 0, 4, s[66:67]
	v_cndmask_b32_e64 v225, 0, 8, vcc
	s_andn2_b64 s[54:55], s[54:55], s[66:67]
	s_andn2_b64 s[56:57], s[56:57], vcc
	v_or3_b32 v228, v228, v224, v225
	v_cmp_ge_f32_e64 s[66:67], v186, v140
	v_cmp_ge_f32_e64 s[58:59], v186, v139
	v_cmp_ge_f32_e32 vcc, v187, v140
	v_cmp_ge_f32_e64 s[60:61], v187, v139
	v_cndmask_b32_e64 v224, 0, v201, s[66:67]
	v_cndmask_b32_e64 v225, 0, v200, vcc
	s_andn2_b64 s[58:59], s[58:59], s[66:67]
	s_andn2_b64 s[60:61], s[60:61], vcc
	v_or3_b32 v228, v228, v224, v225
	v_cmp_ge_f32_e64 s[66:67], v188, v140
	v_cmp_ge_f32_e64 s[62:63], v188, v139
	v_cmp_ge_f32_e32 vcc, v189, v140
	v_cmp_ge_f32_e64 s[64:65], v189, v139
	v_cndmask_b32_e64 v224, 0, v199, s[66:67]
	v_cndmask_b32_e64 v225, 0, v198, vcc
	s_andn2_b64 s[62:63], s[62:63], s[66:67]
	s_andn2_b64 s[64:65], s[64:65], vcc
	v_or3_b32 v228, v228, v224, v225
	v_lshlrev_b32_e32 v104, v143, v228
	ds_bpermute_b32 v105, v144, v104
	v_mov_b32_e32 v227, s96
	s_mov_b64 s[14:15], exec
	s_mov_b64 exec, s[50:51]
	ds_add_rtn_u32 v214, v142, v193
	s_mov_b64 exec, s[52:53]
	ds_add_rtn_u32 v215, v142, v193
	s_mov_b64 exec, s[54:55]
	ds_add_rtn_u32 v216, v142, v193
	s_mov_b64 exec, s[56:57]
	ds_add_rtn_u32 v217, v142, v193
	s_mov_b64 exec, s[58:59]
	ds_add_rtn_u32 v218, v142, v193
	s_mov_b64 exec, s[60:61]
	ds_add_rtn_u32 v219, v142, v193
	s_mov_b64 exec, s[62:63]
	ds_add_rtn_u32 v220, v142, v193
	s_mov_b64 exec, s[64:65]
	ds_add_rtn_u32 v221, v142, v193
	s_mov_b64 exec, s[50:51]
	v_xor_b32_e32 v206, v196, v164
	v_bfe_u32 v222, v206, 11, 10
	v_bfe_u32 v223, v206, 10, 1
	v_lshl_add_u32 v222, v222, 2, v128
	v_mad_u32_u24 v223, v223, v235, 1
	ds_add_u32 v222, v223
	s_mov_b64 exec, s[52:53]
	v_xor_b32_e32 v207, v196, v165
	v_bfe_u32 v222, v207, 11, 10
	v_bfe_u32 v223, v207, 10, 1
	v_lshl_add_u32 v222, v222, 2, v128
	v_mad_u32_u24 v223, v223, v235, 1
	ds_add_u32 v222, v223
	s_mov_b64 exec, s[54:55]
	v_xor_b32_e32 v208, v196, v166
	v_bfe_u32 v222, v208, 11, 10
	v_bfe_u32 v223, v208, 10, 1
	v_lshl_add_u32 v222, v222, 2, v128
	v_mad_u32_u24 v223, v223, v235, 1
	ds_add_u32 v222, v223
	s_mov_b64 exec, s[56:57]
	v_xor_b32_e32 v209, v196, v167
	v_bfe_u32 v222, v209, 11, 10
	v_bfe_u32 v223, v209, 10, 1
	v_lshl_add_u32 v222, v222, 2, v128
	v_mad_u32_u24 v223, v223, v235, 1
	ds_add_u32 v222, v223
	s_waitcnt lgkmcnt(8)
	s_mov_b64 exec, s[58:59]
	v_xor_b32_e32 v210, v196, v186
	v_bfe_u32 v222, v210, 11, 10
	v_bfe_u32 v223, v210, 10, 1
	v_lshl_add_u32 v222, v222, 2, v128
	v_mad_u32_u24 v223, v223, v235, 1
	ds_add_u32 v222, v223
	s_mov_b64 exec, s[60:61]
	v_xor_b32_e32 v211, v196, v187
	v_bfe_u32 v222, v211, 11, 10
	v_bfe_u32 v223, v211, 10, 1
	v_lshl_add_u32 v222, v222, 2, v128
	v_mad_u32_u24 v223, v223, v235, 1
	ds_add_u32 v222, v223
	s_mov_b64 exec, s[62:63]
	v_xor_b32_e32 v212, v196, v188
	v_bfe_u32 v222, v212, 11, 10
	v_bfe_u32 v223, v212, 10, 1
	v_lshl_add_u32 v222, v222, 2, v128
	v_mad_u32_u24 v223, v223, v235, 1
	ds_add_u32 v222, v223
	s_mov_b64 exec, s[64:65]
	v_xor_b32_e32 v213, v196, v189
	v_bfe_u32 v222, v213, 11, 10
	v_bfe_u32 v223, v213, 10, 1
	v_lshl_add_u32 v222, v222, 2, v128
	v_mad_u32_u24 v223, v223, v235, 1
	ds_add_u32 v222, v223
	s_waitcnt lgkmcnt(8)
	s_mov_b64 exec, s[14:15]
	v_or_b32_e32 v104, v105, v104
	ds_bpermute_b32 v105, v145, v104
	s_mov_b64 exec, s[50:51]
	v_cmp_lt_u32_e64 s[66:67], s0, v214
	s_add_i32 s85, s74, 0x0
	v_bfe_u32 v224, v206, 10, 11
	v_lshl_add_u32 v222, v214, 2, v141
	v_add3_u32 v224, v224, v124, s85
	s_andn2_b64 exec, exec, s[66:67]
	ds_write_b32 v222, v224
	s_mov_b64 exec, s[66:67]
	ds_write_b32 v227, v193
	s_mov_b64 exec, s[52:53]
	v_cmp_lt_u32_e64 s[66:67], s0, v215
	s_add_i32 s85, s74, 0x800
	v_bfe_u32 v224, v207, 10, 11
	v_lshl_add_u32 v222, v215, 2, v141
	v_add3_u32 v224, v224, v124, s85
	s_andn2_b64 exec, exec, s[66:67]
	ds_write_b32 v222, v224
	s_mov_b64 exec, s[66:67]
	ds_write_b32 v227, v193
	s_waitcnt lgkmcnt(8)
	s_mov_b64 exec, s[54:55]
	v_cmp_lt_u32_e64 s[66:67], s0, v216
	s_add_i32 s85, s74, 0x1000
	v_bfe_u32 v224, v208, 10, 11
	v_lshl_add_u32 v222, v216, 2, v141
	v_add3_u32 v224, v224, v124, s85
	s_andn2_b64 exec, exec, s[66:67]
	ds_write_b32 v222, v224
	s_mov_b64 exec, s[66:67]
	ds_write_b32 v227, v193
	s_mov_b64 exec, s[56:57]
	v_cmp_lt_u32_e64 s[66:67], s0, v217
	s_add_i32 s85, s74, 0x1800
	v_bfe_u32 v224, v209, 10, 11
	v_lshl_add_u32 v222, v217, 2, v141
	v_add3_u32 v224, v224, v124, s85
	s_andn2_b64 exec, exec, s[66:67]
	ds_write_b32 v222, v224
	s_mov_b64 exec, s[66:67]
	ds_write_b32 v227, v193
	s_waitcnt lgkmcnt(8)
	s_mov_b64 exec, s[58:59]
	v_cmp_lt_u32_e64 s[66:67], s0, v218
	s_add_i32 s85, s74, 0x8000
	v_bfe_u32 v224, v210, 10, 11
	v_lshl_add_u32 v222, v218, 2, v141
	v_add3_u32 v224, v224, v124, s85
	s_andn2_b64 exec, exec, s[66:67]
	ds_write_b32 v222, v224
	s_mov_b64 exec, s[66:67]
	ds_write_b32 v227, v193
	s_mov_b64 exec, s[60:61]
	v_cmp_lt_u32_e64 s[66:67], s0, v219
	s_add_i32 s85, s74, 0x8800
	v_bfe_u32 v224, v211, 10, 11
	v_lshl_add_u32 v222, v219, 2, v141
	v_add3_u32 v224, v224, v124, s85
	s_andn2_b64 exec, exec, s[66:67]
	ds_write_b32 v222, v224
	s_mov_b64 exec, s[66:67]
	ds_write_b32 v227, v193
	s_waitcnt lgkmcnt(8)
	s_mov_b64 exec, s[62:63]
	v_cmp_lt_u32_e64 s[66:67], s0, v220
	s_add_i32 s85, s74, 0x9000
	v_bfe_u32 v224, v212, 10, 11
	v_lshl_add_u32 v222, v220, 2, v141
	v_add3_u32 v224, v224, v124, s85
	s_andn2_b64 exec, exec, s[66:67]
	ds_write_b32 v222, v224
	s_mov_b64 exec, s[66:67]
	ds_write_b32 v227, v193
	s_mov_b64 exec, s[64:65]
	v_cmp_lt_u32_e64 s[66:67], s0, v221
	s_add_i32 s85, s74, 0x9800
	v_bfe_u32 v224, v213, 10, 11
	v_lshl_add_u32 v222, v221, 2, v141
	v_add3_u32 v224, v224, v124, s85
	s_andn2_b64 exec, exec, s[66:67]
	ds_write_b32 v222, v224
	s_mov_b64 exec, s[66:67]
	ds_write_b32 v227, v193
	s_mov_b64 exec, s[14:15]
	s_and_saveexec_b64 s[14:15], s[38:39]
	v_or_b32_e32 v106, v104, v105
	v_lshl_add_u64 v[104:105], v[122:123], 0, s[74:75]
	v_add_co_u32_e32 v104, vcc, 0x3f700000, v104
	s_nop 1
	v_addc_co_u32_e32 v105, vcc, 0, v105, vcc
	global_store_dword v[104:105], v106, off
	s_or_b64 exec, exec, s[14:15]
	s_add_u32 s74, s74, 0x80000
	s_addc_u32 s75, s75, 0
	s_add_i32 s31, s31, 8
	s_cmp_ge_i32 s31, s32
	s_cbranch_scc1 .Lpb2_done
.Lpb2_i2:
	s_add_i32 s85, s31, 32
	s_min_i32 s85, s85, s100
	s_mul_i32 s85, s85, 0x600
	v_add_u32_e32 v233, s85, v230
	v_add_u32_e32 v226, s85, v197
	global_load_dwordx4 v[178:181], v233, s[20:21]
	global_load_dwordx2 v[182:183], v226, s[20:21]
	s_waitcnt vmcnt(12)
	v_perm_b32 v164, v236, v236, v155
	v_perm_b32 v165, v237, v236, v168
	v_perm_b32 v166, v238, v237, v169
	v_perm_b32 v167, v238, v238, v170
	v_perm_b32 v186, v239, v239, v155
	v_perm_b32 v187, v240, v239, v168
	v_perm_b32 v188, v241, v240, v169
	v_perm_b32 v189, v241, v241, v170
	v_cmp_ge_f32_e64 s[66:67], v164, v140
	v_cmp_ge_f32_e64 s[50:51], v164, v139
	v_cmp_ge_f32_e32 vcc, v165, v140
	v_cmp_ge_f32_e64 s[52:53], v165, v139
	v_cndmask_b32_e64 v224, 0, 1, s[66:67]
	v_cndmask_b32_e64 v225, 0, 2, vcc
	s_andn2_b64 s[50:51], s[50:51], s[66:67]
	s_andn2_b64 s[52:53], s[52:53], vcc
	v_or_b32_e32 v228, v224, v225
	v_cmp_ge_f32_e64 s[66:67], v166, v140
	v_cmp_ge_f32_e64 s[54:55], v166, v139
	v_cmp_ge_f32_e32 vcc, v167, v140
	v_cmp_ge_f32_e64 s[56:57], v167, v139
	v_cndmask_b32_e64 v224, 0, 4, s[66:67]
	v_cndmask_b32_e64 v225, 0, 8, vcc
	s_andn2_b64 s[54:55], s[54:55], s[66:67]
	s_andn2_b64 s[56:57], s[56:57], vcc
	v_or3_b32 v228, v228, v224, v225
	v_cmp_ge_f32_e64 s[66:67], v186, v140
	v_cmp_ge_f32_e64 s[58:59], v186, v139
	v_cmp_ge_f32_e32 vcc, v187, v140
	v_cmp_ge_f32_e64 s[60:61], v187, v139
	v_cndmask_b32_e64 v224, 0, v201, s[66:67]
	v_cndmask_b32_e64 v225, 0, v200, vcc
	s_andn2_b64 s[58:59], s[58:59], s[66:67]
	s_andn2_b64 s[60:61], s[60:61], vcc
	v_or3_b32 v228, v228, v224, v225
	v_cmp_ge_f32_e64 s[66:67], v188, v140
	v_cmp_ge_f32_e64 s[62:63], v188, v139
	v_cmp_ge_f32_e32 vcc, v189, v140
	v_cmp_ge_f32_e64 s[64:65], v189, v139
	v_cndmask_b32_e64 v224, 0, v199, s[66:67]
	v_cndmask_b32_e64 v225, 0, v198, vcc
	s_andn2_b64 s[62:63], s[62:63], s[66:67]
	s_andn2_b64 s[64:65], s[64:65], vcc
	v_or3_b32 v228, v228, v224, v225
	v_lshlrev_b32_e32 v104, v143, v228
	ds_bpermute_b32 v105, v144, v104
	v_mov_b32_e32 v227, s96
	s_mov_b64 s[14:15], exec
	s_mov_b64 exec, s[50:51]
	ds_add_rtn_u32 v214, v142, v193
	s_mov_b64 exec, s[52:53]
	ds_add_rtn_u32 v215, v142, v193
	s_mov_b64 exec, s[54:55]
	ds_add_rtn_u32 v216, v142, v193
	s_mov_b64 exec, s[56:57]
	ds_add_rtn_u32 v217, v142, v193
	s_mov_b64 exec, s[58:59]
	ds_add_rtn_u32 v218, v142, v193
	s_mov_b64 exec, s[60:61]
	ds_add_rtn_u32 v219, v142, v193
	s_mov_b64 exec, s[62:63]
	ds_add_rtn_u32 v220, v142, v193
	s_mov_b64 exec, s[64:65]
	ds_add_rtn_u32 v221, v142, v193
	s_mov_b64 exec, s[50:51]
	v_xor_b32_e32 v206, v196, v164
	v_bfe_u32 v222, v206, 11, 10
	v_bfe_u32 v223, v206, 10, 1
	v_lshl_add_u32 v222, v222, 2, v128
	v_mad_u32_u24 v223, v223, v235, 1
	ds_add_u32 v222, v223
	s_mov_b64 exec, s[52:53]
	v_xor_b32_e32 v207, v196, v165
	v_bfe_u32 v222, v207, 11, 10
	v_bfe_u32 v223, v207, 10, 1
	v_lshl_add_u32 v222, v222, 2, v128
	v_mad_u32_u24 v223, v223, v235, 1
	ds_add_u32 v222, v223
	s_mov_b64 exec, s[54:55]
	v_xor_b32_e32 v208, v196, v166
	v_bfe_u32 v222, v208, 11, 10
	v_bfe_u32 v223, v208, 10, 1
	v_lshl_add_u32 v222, v222, 2, v128
	v_mad_u32_u24 v223, v223, v235, 1
	ds_add_u32 v222, v223
	s_mov_b64 exec, s[56:57]
	v_xor_b32_e32 v209, v196, v167
	v_bfe_u32 v222, v209, 11, 10
	v_bfe_u32 v223, v209, 10, 1
	v_lshl_add_u32 v222, v222, 2, v128
	v_mad_u32_u24 v223, v223, v235, 1
	ds_add_u32 v222, v223
	s_waitcnt lgkmcnt(8)
	s_mov_b64 exec, s[58:59]
	v_xor_b32_e32 v210, v196, v186
	v_bfe_u32 v222, v210, 11, 10
	v_bfe_u32 v223, v210, 10, 1
	v_lshl_add_u32 v222, v222, 2, v128
	v_mad_u32_u24 v223, v223, v235, 1
	ds_add_u32 v222, v223
	s_mov_b64 exec, s[60:61]
	v_xor_b32_e32 v211, v196, v187
	v_bfe_u32 v222, v211, 11, 10
	v_bfe_u32 v223, v211, 10, 1
	v_lshl_add_u32 v222, v222, 2, v128
	v_mad_u32_u24 v223, v223, v235, 1
	ds_add_u32 v222, v223
	s_mov_b64 exec, s[62:63]
	v_xor_b32_e32 v212, v196, v188
	v_bfe_u32 v222, v212, 11, 10
	v_bfe_u32 v223, v212, 10, 1
	v_lshl_add_u32 v222, v222, 2, v128
	v_mad_u32_u24 v223, v223, v235, 1
	ds_add_u32 v222, v223
	s_mov_b64 exec, s[64:65]
	v_xor_b32_e32 v213, v196, v189
	v_bfe_u32 v222, v213, 11, 10
	v_bfe_u32 v223, v213, 10, 1
	v_lshl_add_u32 v222, v222, 2, v128
	v_mad_u32_u24 v223, v223, v235, 1
	ds_add_u32 v222, v223
	s_waitcnt lgkmcnt(8)
	s_mov_b64 exec, s[14:15]
	v_or_b32_e32 v104, v105, v104
	ds_bpermute_b32 v105, v145, v104
	s_mov_b64 exec, s[50:51]
	v_cmp_lt_u32_e64 s[66:67], s0, v214
	s_add_i32 s85, s74, 0x0
	v_bfe_u32 v224, v206, 10, 11
	v_lshl_add_u32 v222, v214, 2, v141
	v_add3_u32 v224, v224, v124, s85
	s_andn2_b64 exec, exec, s[66:67]
	ds_write_b32 v222, v224
	s_mov_b64 exec, s[66:67]
	ds_write_b32 v227, v193
	s_mov_b64 exec, s[52:53]
	v_cmp_lt_u32_e64 s[66:67], s0, v215
	s_add_i32 s85, s74, 0x800
	v_bfe_u32 v224, v207, 10, 11
	v_lshl_add_u32 v222, v215, 2, v141
	v_add3_u32 v224, v224, v124, s85
	s_andn2_b64 exec, exec, s[66:67]
	ds_write_b32 v222, v224
	s_mov_b64 exec, s[66:67]
	ds_write_b32 v227, v193
	s_waitcnt lgkmcnt(8)
	s_mov_b64 exec, s[54:55]
	v_cmp_lt_u32_e64 s[66:67], s0, v216
	s_add_i32 s85, s74, 0x1000
	v_bfe_u32 v224, v208, 10, 11
	v_lshl_add_u32 v222, v216, 2, v141
	v_add3_u32 v224, v224, v124, s85
	s_andn2_b64 exec, exec, s[66:67]
	ds_write_b32 v222, v224
	s_mov_b64 exec, s[66:67]
	ds_write_b32 v227, v193
	s_mov_b64 exec, s[56:57]
	v_cmp_lt_u32_e64 s[66:67], s0, v217
	s_add_i32 s85, s74, 0x1800
	v_bfe_u32 v224, v209, 10, 11
	v_lshl_add_u32 v222, v217, 2, v141
	v_add3_u32 v224, v224, v124, s85
	s_andn2_b64 exec, exec, s[66:67]
	ds_write_b32 v222, v224
	s_mov_b64 exec, s[66:67]
	ds_write_b32 v227, v193
	s_waitcnt lgkmcnt(8)
	s_mov_b64 exec, s[58:59]
	v_cmp_lt_u32_e64 s[66:67], s0, v218
	s_add_i32 s85, s74, 0x8000
	v_bfe_u32 v224, v210, 10, 11
	v_lshl_add_u32 v222, v218, 2, v141
	v_add3_u32 v224, v224, v124, s85
	s_andn2_b64 exec, exec, s[66:67]
	ds_write_b32 v222, v224
	s_mov_b64 exec, s[66:67]
	ds_write_b32 v227, v193
	s_mov_b64 exec, s[60:61]
	v_cmp_lt_u32_e64 s[66:67], s0, v219
	s_add_i32 s85, s74, 0x8800
	v_bfe_u32 v224, v211, 10, 11
	v_lshl_add_u32 v222, v219, 2, v141
	v_add3_u32 v224, v224, v124, s85
	s_andn2_b64 exec, exec, s[66:67]
	ds_write_b32 v222, v224
	s_mov_b64 exec, s[66:67]
	ds_write_b32 v227, v193
	s_waitcnt lgkmcnt(8)
	s_mov_b64 exec, s[62:63]
	v_cmp_lt_u32_e64 s[66:67], s0, v220
	s_add_i32 s85, s74, 0x9000
	v_bfe_u32 v224, v212, 10, 11
	v_lshl_add_u32 v222, v220, 2, v141
	v_add3_u32 v224, v224, v124, s85
	s_andn2_b64 exec, exec, s[66:67]
	ds_write_b32 v222, v224
	s_mov_b64 exec, s[66:67]
	ds_write_b32 v227, v193
	s_mov_b64 exec, s[64:65]
	v_cmp_lt_u32_e64 s[66:67], s0, v221
	s_add_i32 s85, s74, 0x9800
	v_bfe_u32 v224, v213, 10, 11
	v_lshl_add_u32 v222, v221, 2, v141
	v_add3_u32 v224, v224, v124, s85
	s_andn2_b64 exec, exec, s[66:67]
	ds_write_b32 v222, v224
	s_mov_b64 exec, s[66:67]
	ds_write_b32 v227, v193
	s_mov_b64 exec, s[14:15]
	s_and_saveexec_b64 s[14:15], s[38:39]
	v_or_b32_e32 v106, v104, v105
	v_lshl_add_u64 v[104:105], v[122:123], 0, s[74:75]
	v_add_co_u32_e32 v104, vcc, 0x3f700000, v104
	s_nop 1
	v_addc_co_u32_e32 v105, vcc, 0, v105, vcc
	global_store_dword v[104:105], v106, off
	s_or_b64 exec, exec, s[14:15]
	s_add_u32 s74, s74, 0x80000
	s_addc_u32 s75, s75, 0
	s_add_i32 s31, s31, 8
	s_cmp_ge_i32 s31, s32
	s_cbranch_scc1 .Lpb2_done
.Lpb2_i3:
	s_add_i32 s85, s31, 32
	s_min_i32 s85, s85, s100
	s_mul_i32 s85, s85, 0x600
	v_add_u32_e32 v233, s85, v230
	v_add_u32_e32 v226, s85, v197
	global_load_dwordx4 v[236:239], v233, s[20:21]
	global_load_dwordx2 v[240:241], v226, s[20:21]
	s_waitcnt vmcnt(12)
	v_perm_b32 v164, v80, v80, v155
	v_perm_b32 v165, v81, v80, v168
	v_perm_b32 v166, v82, v81, v169
	v_perm_b32 v167, v82, v82, v170
	v_perm_b32 v186, v83, v83, v155
	v_perm_b32 v187, v84, v83, v168
	v_perm_b32 v188, v85, v84, v169
	v_perm_b32 v189, v85, v85, v170
	v_cmp_ge_f32_e64 s[66:67], v164, v140
	v_cmp_ge_f32_e64 s[50:51], v164, v139
	v_cmp_ge_f32_e32 vcc, v165, v140
	v_cmp_ge_f32_e64 s[52:53], v165, v139
	v_cndmask_b32_e64 v224, 0, 1, s[66:67]
	v_cndmask_b32_e64 v225, 0, 2, vcc
	s_andn2_b64 s[50:51], s[50:51], s[66:67]
	s_andn2_b64 s[52:53], s[52:53], vcc
	v_or_b32_e32 v228, v224, v225
	v_cmp_ge_f32_e64 s[66:67], v166, v140
	v_cmp_ge_f32_e64 s[54:55], v166, v139
	v_cmp_ge_f32_e32 vcc, v167, v140
	v_cmp_ge_f32_e64 s[56:57], v167, v139
	v_cndmask_b32_e64 v224, 0, 4, s[66:67]
	v_cndmask_b32_e64 v225, 0, 8, vcc
	s_andn2_b64 s[54:55], s[54:55], s[66:67]
	s_andn2_b64 s[56:57], s[56:57], vcc
	v_or3_b32 v228, v228, v224, v225
	v_cmp_ge_f32_e64 s[66:67], v186, v140
	v_cmp_ge_f32_e64 s[58:59], v186, v139
	v_cmp_ge_f32_e32 vcc, v187, v140
	v_cmp_ge_f32_e64 s[60:61], v187, v139
	v_cndmask_b32_e64 v224, 0, v201, s[66:67]
	v_cndmask_b32_e64 v225, 0, v200, vcc
	s_andn2_b64 s[58:59], s[58:59], s[66:67]
	s_andn2_b64 s[60:61], s[60:61], vcc
	v_or3_b32 v228, v228, v224, v225
	v_cmp_ge_f32_e64 s[66:67], v188, v140
	v_cmp_ge_f32_e64 s[62:63], v188, v139
	v_cmp_ge_f32_e32 vcc, v189, v140
	v_cmp_ge_f32_e64 s[64:65], v189, v139
	v_cndmask_b32_e64 v224, 0, v199, s[66:67]
	v_cndmask_b32_e64 v225, 0, v198, vcc
	s_andn2_b64 s[62:63], s[62:63], s[66:67]
	s_andn2_b64 s[64:65], s[64:65], vcc
	v_or3_b32 v228, v228, v224, v225
	v_lshlrev_b32_e32 v104, v143, v228
	ds_bpermute_b32 v105, v144, v104
	v_mov_b32_e32 v227, s96
	s_mov_b64 s[14:15], exec
	s_mov_b64 exec, s[50:51]
	ds_add_rtn_u32 v214, v142, v193
	s_mov_b64 exec, s[52:53]
	ds_add_rtn_u32 v215, v142, v193
	s_mov_b64 exec, s[54:55]
	ds_add_rtn_u32 v216, v142, v193
	s_mov_b64 exec, s[56:57]
	ds_add_rtn_u32 v217, v142, v193
	s_mov_b64 exec, s[58:59]
	ds_add_rtn_u32 v218, v142, v193
	s_mov_b64 exec, s[60:61]
	ds_add_rtn_u32 v219, v142, v193
	s_mov_b64 exec, s[62:63]
	ds_add_rtn_u32 v220, v142, v193
	s_mov_b64 exec, s[64:65]
	ds_add_rtn_u32 v221, v142, v193
	s_mov_b64 exec, s[50:51]
	v_xor_b32_e32 v206, v196, v164
	v_bfe_u32 v222, v206, 11, 10
	v_bfe_u32 v223, v206, 10, 1
	v_lshl_add_u32 v222, v222, 2, v128
	v_mad_u32_u24 v223, v223, v235, 1
	ds_add_u32 v222, v223
	s_mov_b64 exec, s[52:53]
	v_xor_b32_e32 v207, v196, v165
	v_bfe_u32 v222, v207, 11, 10
	v_bfe_u32 v223, v207, 10, 1
	v_lshl_add_u32 v222, v222, 2, v128
	v_mad_u32_u24 v223, v223, v235, 1
	ds_add_u32 v222, v223
	s_mov_b64 exec, s[54:55]
	v_xor_b32_e32 v208, v196, v166
	v_bfe_u32 v222, v208, 11, 10
	v_bfe_u32 v223, v208, 10, 1
	v_lshl_add_u32 v222, v222, 2, v128
	v_mad_u32_u24 v223, v223, v235, 1
	ds_add_u32 v222, v223
	s_mov_b64 exec, s[56:57]
	v_xor_b32_e32 v209, v196, v167
	v_bfe_u32 v222, v209, 11, 10
	v_bfe_u32 v223, v209, 10, 1
	v_lshl_add_u32 v222, v222, 2, v128
	v_mad_u32_u24 v223, v223, v235, 1
	ds_add_u32 v222, v223
	s_waitcnt lgkmcnt(8)
	s_mov_b64 exec, s[58:59]
	v_xor_b32_e32 v210, v196, v186
	v_bfe_u32 v222, v210, 11, 10
	v_bfe_u32 v223, v210, 10, 1
	v_lshl_add_u32 v222, v222, 2, v128
	v_mad_u32_u24 v223, v223, v235, 1
	ds_add_u32 v222, v223
	s_mov_b64 exec, s[60:61]
	v_xor_b32_e32 v211, v196, v187
	v_bfe_u32 v222, v211, 11, 10
	v_bfe_u32 v223, v211, 10, 1
	v_lshl_add_u32 v222, v222, 2, v128
	v_mad_u32_u24 v223, v223, v235, 1
	ds_add_u32 v222, v223
	s_mov_b64 exec, s[62:63]
	v_xor_b32_e32 v212, v196, v188
	v_bfe_u32 v222, v212, 11, 10
	v_bfe_u32 v223, v212, 10, 1
	v_lshl_add_u32 v222, v222, 2, v128
	v_mad_u32_u24 v223, v223, v235, 1
	ds_add_u32 v222, v223
	s_mov_b64 exec, s[64:65]
	v_xor_b32_e32 v213, v196, v189
	v_bfe_u32 v222, v213, 11, 10
	v_bfe_u32 v223, v213, 10, 1
	v_lshl_add_u32 v222, v222, 2, v128
	v_mad_u32_u24 v223, v223, v235, 1
	ds_add_u32 v222, v223
	s_waitcnt lgkmcnt(8)
	s_mov_b64 exec, s[14:15]
	v_or_b32_e32 v104, v105, v104
	ds_bpermute_b32 v105, v145, v104
	s_mov_b64 exec, s[50:51]
	v_cmp_lt_u32_e64 s[66:67], s0, v214
	s_add_i32 s85, s74, 0x0
	v_bfe_u32 v224, v206, 10, 11
	v_lshl_add_u32 v222, v214, 2, v141
	v_add3_u32 v224, v224, v124, s85
	s_andn2_b64 exec, exec, s[66:67]
	ds_write_b32 v222, v224
	s_mov_b64 exec, s[66:67]
	ds_write_b32 v227, v193
	s_mov_b64 exec, s[52:53]
	v_cmp_lt_u32_e64 s[66:67], s0, v215
	s_add_i32 s85, s74, 0x800
	v_bfe_u32 v224, v207, 10, 11
	v_lshl_add_u32 v222, v215, 2, v141
	v_add3_u32 v224, v224, v124, s85
	s_andn2_b64 exec, exec, s[66:67]
	ds_write_b32 v222, v224
	s_mov_b64 exec, s[66:67]
	ds_write_b32 v227, v193
	s_waitcnt lgkmcnt(8)
	s_mov_b64 exec, s[54:55]
	v_cmp_lt_u32_e64 s[66:67], s0, v216
	s_add_i32 s85, s74, 0x1000
	v_bfe_u32 v224, v208, 10, 11
	v_lshl_add_u32 v222, v216, 2, v141
	v_add3_u32 v224, v224, v124, s85
	s_andn2_b64 exec, exec, s[66:67]
	ds_write_b32 v222, v224
	s_mov_b64 exec, s[66:67]
	ds_write_b32 v227, v193
	s_mov_b64 exec, s[56:57]
	v_cmp_lt_u32_e64 s[66:67], s0, v217
	s_add_i32 s85, s74, 0x1800
	v_bfe_u32 v224, v209, 10, 11
	v_lshl_add_u32 v222, v217, 2, v141
	v_add3_u32 v224, v224, v124, s85
	s_andn2_b64 exec, exec, s[66:67]
	ds_write_b32 v222, v224
	s_mov_b64 exec, s[66:67]
	ds_write_b32 v227, v193
	s_waitcnt lgkmcnt(8)
	s_mov_b64 exec, s[58:59]
	v_cmp_lt_u32_e64 s[66:67], s0, v218
	s_add_i32 s85, s74, 0x8000
	v_bfe_u32 v224, v210, 10, 11
	v_lshl_add_u32 v222, v218, 2, v141
	v_add3_u32 v224, v224, v124, s85
	s_andn2_b64 exec, exec, s[66:67]
	ds_write_b32 v222, v224
	s_mov_b64 exec, s[66:67]
	ds_write_b32 v227, v193
	s_mov_b64 exec, s[60:61]
	v_cmp_lt_u32_e64 s[66:67], s0, v219
	s_add_i32 s85, s74, 0x8800
	v_bfe_u32 v224, v211, 10, 11
	v_lshl_add_u32 v222, v219, 2, v141
	v_add3_u32 v224, v224, v124, s85
	s_andn2_b64 exec, exec, s[66:67]
	ds_write_b32 v222, v224
	s_mov_b64 exec, s[66:67]
	ds_write_b32 v227, v193
	s_waitcnt lgkmcnt(8)
	s_mov_b64 exec, s[62:63]
	v_cmp_lt_u32_e64 s[66:67], s0, v220
	s_add_i32 s85, s74, 0x9000
	v_bfe_u32 v224, v212, 10, 11
	v_lshl_add_u32 v222, v220, 2, v141
	v_add3_u32 v224, v224, v124, s85
	s_andn2_b64 exec, exec, s[66:67]
	ds_write_b32 v222, v224
	s_mov_b64 exec, s[66:67]
	ds_write_b32 v227, v193
	s_mov_b64 exec, s[64:65]
	v_cmp_lt_u32_e64 s[66:67], s0, v221
	s_add_i32 s85, s74, 0x9800
	v_bfe_u32 v224, v213, 10, 11
	v_lshl_add_u32 v222, v221, 2, v141
	v_add3_u32 v224, v224, v124, s85
	s_andn2_b64 exec, exec, s[66:67]
	ds_write_b32 v222, v224
	s_mov_b64 exec, s[66:67]
	ds_write_b32 v227, v193
	s_mov_b64 exec, s[14:15]
	s_and_saveexec_b64 s[14:15], s[38:39]
	v_or_b32_e32 v106, v104, v105
	v_lshl_add_u64 v[104:105], v[122:123], 0, s[74:75]
	v_add_co_u32_e32 v104, vcc, 0x3f700000, v104
	s_nop 1
	v_addc_co_u32_e32 v105, vcc, 0, v105, vcc
	global_store_dword v[104:105], v106, off
	s_or_b64 exec, exec, s[14:15]
	s_add_u32 s74, s74, 0x80000
	s_addc_u32 s75, s75, 0
	s_add_i32 s31, s31, 8
	s_cmp_ge_i32 s31, s32
	s_cbranch_scc1 .Lpb2_done
.Lpb2_i4:
	s_add_i32 s85, s31, 32
	s_min_i32 s85, s85, s100
	s_mul_i32 s85, s85, 0x600
	v_add_u32_e32 v233, s85, v230
	v_add_u32_e32 v226, s85, v197
	global_load_dwordx4 v[80:83], v233, s[20:21]
	global_load_dwordx2 v[84:85], v226, s[20:21]
	s_waitcnt vmcnt(12)
	v_perm_b32 v164, v72, v72, v155
	v_perm_b32 v165, v73, v72, v168
	v_perm_b32 v166, v74, v73, v169
	v_perm_b32 v167, v74, v74, v170
	v_perm_b32 v186, v75, v75, v155
	v_perm_b32 v187, v76, v75, v168
	v_perm_b32 v188, v77, v76, v169
	v_perm_b32 v189, v77, v77, v170
	v_cmp_ge_f32_e64 s[66:67], v164, v140
	v_cmp_ge_f32_e64 s[50:51], v164, v139
	v_cmp_ge_f32_e32 vcc, v165, v140
	v_cmp_ge_f32_e64 s[52:53], v165, v139
	v_cndmask_b32_e64 v224, 0, 1, s[66:67]
	v_cndmask_b32_e64 v225, 0, 2, vcc
	s_andn2_b64 s[50:51], s[50:51], s[66:67]
	s_andn2_b64 s[52:53], s[52:53], vcc
	v_or_b32_e32 v228, v224, v225
	v_cmp_ge_f32_e64 s[66:67], v166, v140
	v_cmp_ge_f32_e64 s[54:55], v166, v139
	v_cmp_ge_f32_e32 vcc, v167, v140
	v_cmp_ge_f32_e64 s[56:57], v167, v139
	v_cndmask_b32_e64 v224, 0, 4, s[66:67]
	v_cndmask_b32_e64 v225, 0, 8, vcc
	s_andn2_b64 s[54:55], s[54:55], s[66:67]
	s_andn2_b64 s[56:57], s[56:57], vcc
	v_or3_b32 v228, v228, v224, v225
	v_cmp_ge_f32_e64 s[66:67], v186, v140
	v_cmp_ge_f32_e64 s[58:59], v186, v139
	v_cmp_ge_f32_e32 vcc, v187, v140
	v_cmp_ge_f32_e64 s[60:61], v187, v139
	v_cndmask_b32_e64 v224, 0, v201, s[66:67]
	v_cndmask_b32_e64 v225, 0, v200, vcc
	s_andn2_b64 s[58:59], s[58:59], s[66:67]
	s_andn2_b64 s[60:61], s[60:61], vcc
	v_or3_b32 v228, v228, v224, v225
	v_cmp_ge_f32_e64 s[66:67], v188, v140
	v_cmp_ge_f32_e64 s[62:63], v188, v139
	v_cmp_ge_f32_e32 vcc, v189, v140
	v_cmp_ge_f32_e64 s[64:65], v189, v139
	v_cndmask_b32_e64 v224, 0, v199, s[66:67]
	v_cndmask_b32_e64 v225, 0, v198, vcc
	s_andn2_b64 s[62:63], s[62:63], s[66:67]
	s_andn2_b64 s[64:65], s[64:65], vcc
	v_or3_b32 v228, v228, v224, v225
	v_lshlrev_b32_e32 v104, v143, v228
	ds_bpermute_b32 v105, v144, v104
	v_mov_b32_e32 v227, s96
	s_mov_b64 s[14:15], exec
	s_mov_b64 exec, s[50:51]
	ds_add_rtn_u32 v214, v142, v193
	s_mov_b64 exec, s[52:53]
	ds_add_rtn_u32 v215, v142, v193
	s_mov_b64 exec, s[54:55]
	ds_add_rtn_u32 v216, v142, v193
	s_mov_b64 exec, s[56:57]
	ds_add_rtn_u32 v217, v142, v193
	s_mov_b64 exec, s[58:59]
	ds_add_rtn_u32 v218, v142, v193
	s_mov_b64 exec, s[60:61]
	ds_add_rtn_u32 v219, v142, v193
	s_mov_b64 exec, s[62:63]
	ds_add_rtn_u32 v220, v142, v193
	s_mov_b64 exec, s[64:65]
	ds_add_rtn_u32 v221, v142, v193
	s_mov_b64 exec, s[50:51]
	v_xor_b32_e32 v206, v196, v164
	v_bfe_u32 v222, v206, 11, 10
	v_bfe_u32 v223, v206, 10, 1
	v_lshl_add_u32 v222, v222, 2, v128
	v_mad_u32_u24 v223, v223, v235, 1
	ds_add_u32 v222, v223
	s_mov_b64 exec, s[52:53]
	v_xor_b32_e32 v207, v196, v165
	v_bfe_u32 v222, v207, 11, 10
	v_bfe_u32 v223, v207, 10, 1
	v_lshl_add_u32 v222, v222, 2, v128
	v_mad_u32_u24 v223, v223, v235, 1
	ds_add_u32 v222, v223
	s_mov_b64 exec, s[54:55]
	v_xor_b32_e32 v208, v196, v166
	v_bfe_u32 v222, v208, 11, 10
	v_bfe_u32 v223, v208, 10, 1
	v_lshl_add_u32 v222, v222, 2, v128
	v_mad_u32_u24 v223, v223, v235, 1
	ds_add_u32 v222, v223
	s_mov_b64 exec, s[56:57]
	v_xor_b32_e32 v209, v196, v167
	v_bfe_u32 v222, v209, 11, 10
	v_bfe_u32 v223, v209, 10, 1
	v_lshl_add_u32 v222, v222, 2, v128
	v_mad_u32_u24 v223, v223, v235, 1
	ds_add_u32 v222, v223
	s_waitcnt lgkmcnt(8)
	s_mov_b64 exec, s[58:59]
	v_xor_b32_e32 v210, v196, v186
	v_bfe_u32 v222, v210, 11, 10
	v_bfe_u32 v223, v210, 10, 1
	v_lshl_add_u32 v222, v222, 2, v128
	v_mad_u32_u24 v223, v223, v235, 1
	ds_add_u32 v222, v223
	s_mov_b64 exec, s[60:61]
	v_xor_b32_e32 v211, v196, v187
	v_bfe_u32 v222, v211, 11, 10
	v_bfe_u32 v223, v211, 10, 1
	v_lshl_add_u32 v222, v222, 2, v128
	v_mad_u32_u24 v223, v223, v235, 1
	ds_add_u32 v222, v223
	s_mov_b64 exec, s[62:63]
	v_xor_b32_e32 v212, v196, v188
	v_bfe_u32 v222, v212, 11, 10
	v_bfe_u32 v223, v212, 10, 1
	v_lshl_add_u32 v222, v222, 2, v128
	v_mad_u32_u24 v223, v223, v235, 1
	ds_add_u32 v222, v223
	s_mov_b64 exec, s[64:65]
	v_xor_b32_e32 v213, v196, v189
	v_bfe_u32 v222, v213, 11, 10
	v_bfe_u32 v223, v213, 10, 1
	v_lshl_add_u32 v222, v222, 2, v128
	v_mad_u32_u24 v223, v223, v235, 1
	ds_add_u32 v222, v223
	s_waitcnt lgkmcnt(8)
	s_mov_b64 exec, s[14:15]
	v_or_b32_e32 v104, v105, v104
	ds_bpermute_b32 v105, v145, v104
	s_mov_b64 exec, s[50:51]
	v_cmp_lt_u32_e64 s[66:67], s0, v214
	s_add_i32 s85, s74, 0x0
	v_bfe_u32 v224, v206, 10, 11
	v_lshl_add_u32 v222, v214, 2, v141
	v_add3_u32 v224, v224, v124, s85
	s_andn2_b64 exec, exec, s[66:67]
	ds_write_b32 v222, v224
	s_mov_b64 exec, s[66:67]
	ds_write_b32 v227, v193
	s_mov_b64 exec, s[52:53]
	v_cmp_lt_u32_e64 s[66:67], s0, v215
	s_add_i32 s85, s74, 0x800
	v_bfe_u32 v224, v207, 10, 11
	v_lshl_add_u32 v222, v215, 2, v141
	v_add3_u32 v224, v224, v124, s85
	s_andn2_b64 exec, exec, s[66:67]
	ds_write_b32 v222, v224
	s_mov_b64 exec, s[66:67]
	ds_write_b32 v227, v193
	s_waitcnt lgkmcnt(8)
	s_mov_b64 exec, s[54:55]
	v_cmp_lt_u32_e64 s[66:67], s0, v216
	s_add_i32 s85, s74, 0x1000
	v_bfe_u32 v224, v208, 10, 11
	v_lshl_add_u32 v222, v216, 2, v141
	v_add3_u32 v224, v224, v124, s85
	s_andn2_b64 exec, exec, s[66:67]
	ds_write_b32 v222, v224
	s_mov_b64 exec, s[66:67]
	ds_write_b32 v227, v193
	s_mov_b64 exec, s[56:57]
	v_cmp_lt_u32_e64 s[66:67], s0, v217
	s_add_i32 s85, s74, 0x1800
	v_bfe_u32 v224, v209, 10, 11
	v_lshl_add_u32 v222, v217, 2, v141
	v_add3_u32 v224, v224, v124, s85
	s_andn2_b64 exec, exec, s[66:67]
	ds_write_b32 v222, v224
	s_mov_b64 exec, s[66:67]
	ds_write_b32 v227, v193
	s_waitcnt lgkmcnt(8)
	s_mov_b64 exec, s[58:59]
	v_cmp_lt_u32_e64 s[66:67], s0, v218
	s_add_i32 s85, s74, 0x8000
	v_bfe_u32 v224, v210, 10, 11
	v_lshl_add_u32 v222, v218, 2, v141
	v_add3_u32 v224, v224, v124, s85
	s_andn2_b64 exec, exec, s[66:67]
	ds_write_b32 v222, v224
	s_mov_b64 exec, s[66:67]
	ds_write_b32 v227, v193
	s_mov_b64 exec, s[60:61]
	v_cmp_lt_u32_e64 s[66:67], s0, v219
	s_add_i32 s85, s74, 0x8800
	v_bfe_u32 v224, v211, 10, 11
	v_lshl_add_u32 v222, v219, 2, v141
	v_add3_u32 v224, v224, v124, s85
	s_andn2_b64 exec, exec, s[66:67]
	ds_write_b32 v222, v224
	s_mov_b64 exec, s[66:67]
	ds_write_b32 v227, v193
	s_waitcnt lgkmcnt(8)
	s_mov_b64 exec, s[62:63]
	v_cmp_lt_u32_e64 s[66:67], s0, v220
	s_add_i32 s85, s74, 0x9000
	v_bfe_u32 v224, v212, 10, 11
	v_lshl_add_u32 v222, v220, 2, v141
	v_add3_u32 v224, v224, v124, s85
	s_andn2_b64 exec, exec, s[66:67]
	ds_write_b32 v222, v224
	s_mov_b64 exec, s[66:67]
	ds_write_b32 v227, v193
	s_mov_b64 exec, s[64:65]
	v_cmp_lt_u32_e64 s[66:67], s0, v221
	s_add_i32 s85, s74, 0x9800
	v_bfe_u32 v224, v213, 10, 11
	v_lshl_add_u32 v222, v221, 2, v141
	v_add3_u32 v224, v224, v124, s85
	s_andn2_b64 exec, exec, s[66:67]
	ds_write_b32 v222, v224
	s_mov_b64 exec, s[66:67]
	ds_write_b32 v227, v193
	s_mov_b64 exec, s[14:15]
	s_and_saveexec_b64 s[14:15], s[38:39]
	v_or_b32_e32 v106, v104, v105
	v_lshl_add_u64 v[104:105], v[122:123], 0, s[74:75]
	v_add_co_u32_e32 v104, vcc, 0x3f700000, v104
	s_nop 1
	v_addc_co_u32_e32 v105, vcc, 0, v105, vcc
	global_store_dword v[104:105], v106, off
	s_or_b64 exec, exec, s[14:15]
	s_add_u32 s74, s74, 0x80000
	s_addc_u32 s75, s75, 0
	s_add_i32 s31, s31, 8
	s_cmp_ge_i32 s31, s32
	s_cbranch_scc0 .Lpb2_i0
